# expert GEMM K-loops by hand, two barriers per K-tile; the lagging wave group stages the tile after next right after its fragment reads (no instruction between MFMAs)
# speedup vs baseline: 1.0283x; 1.0283x over previous
; #define G_WAIT_V(n) asm volatile("s_waitcnt vmcnt(" #n ")" ::: "memory")
; #define G_BAR() __builtin_amdgcn_s_barrier()
; #define G_SCHED() __builtin_amdgcn_sched_barrier(0)
; #define D_STAGE_A(slot, half, kt) D_STAGE(rsA, voffA, slot, half, kt)
; #define D_STAGE_B(slot, half, kt) D_STAGE(rsB, voffB, slot, half, kt)
; #define D_LDA(dst, slot) do { _Pragma("unroll") for (int m = 0; m < 4; ++m) _Pragma("unroll") for (int k = 0; k < 2; ++k) \
;     dst[m][k] = *(const LDS_AS bf16x8*)(lds + (slot) + aoff + m * 2048 + k * 1024); } while (0)
; #define D_LDB(dst, slot) do { _Pragma("unroll") for (int n = 0; n < 2; ++n) _Pragma("unroll") for (int k = 0; k < 2; ++k) \
;     dst[n][k] = *(const LDS_AS bf16x8*)(lds + (slot) + boff + n * 2048 + k * 1024); } while (0)
; #define D_MMA(ai, bj, At, Bf) do { __builtin_amdgcn_s_setprio(1); _Pragma("unroll") for (int m = 0; m < 4; ++m) _Pragma("unroll") for (int n = 0; n < 2; ++n) _Pragma("unroll") for (int k = 0; k < 2; ++k) \
;     acc[ai][bj][m][n] = __builtin_amdgcn_mfma_f32_16x16x32_bf16(Bf[n][k], At[m][k], acc[ai][bj][m][n], 0, 0, 0); __builtin_amdgcn_s_setprio(0); } while (0)
; #define D_WAIT_L(n) asm volatile("s_waitcnt lgkmcnt(" #n ")" ::: "memory")
; #define D_STAGE_A(slot, half, kt) D_STAGE(rsA, voffA, slot, half, kt)
; #define D_STAGE_B(slot, half, kt) do { _Pragma("unroll") for (int _i = 0; _i < 2; ++_i) { const unsigned _m0 = ldsw + (unsigned)((slot) + _i * 8192); const unsigned _so = (unsigned)(kt) * 128u + (half) * bt_half + _i * bt_piece; \
;     asm volatile("s_mov_b32 m0, %0\n\ts_nop 4\n\tbuffer_load_dwordx4 %1, %2, %3 offen lds" :: "s"(_m0), "v"(voffB0), "s"(rsB), "s"(_so) : "m0", "memory"); } } while (0)
; #define D_WAIT_L(n) asm volatile("s_waitcnt lgkmcnt(" #n ")" ::: "memory")
;     ...
;     D_LDB(B0, G_SB(0, 0)); G_SCHED(); D_LDA(At, G_SA(0, 0)); D_STAGE_A(G_SA(1, 1), 1, t1);
;     D_WAIT_L(8); G_BAR(); D_WAIT_L(0); G_SCHED(); D_MMA(0, 0, At, B0); G_BAR(); G_SCHED();
;     D_LDB(B1, G_SB(0, 1)); D_STAGE_B(G_SB(0, 0), 0, t2);
;     G_BAR(); D_WAIT_L(0); G_SCHED(); D_MMA(0, 1, At, B1); G_BAR(); G_SCHED();
;     D_LDA(At, G_SA(0, 1)); D_STAGE_A(G_SA(0, 0), 0, t2);
;     G_BAR(); D_WAIT_L(0); G_SCHED(); D_MMA(1, 0, At, B0); G_BAR(); G_SCHED();
;     D_STAGE_B(G_SB(0, 1), 1, t2);
;     G_WAIT_V(6); G_BAR(); G_SCHED(); D_MMA(1, 1, At, B1); G_BAR(); G_SCHED();
.Lkl_m1npre_yl:
	ds_read_b128 v[200:203], v130
	ds_read_b128 v[204:207], v131
	ds_read_b128 v[220:223], v130 offset:2048
	ds_read_b128 v[224:227], v131 offset:2048
	ds_read_b128 v[228:231], v132
	ds_read_b128 v[232:235], v133
	ds_read_b128 v[240:243], v132 offset:2048
	ds_read_b128 v[244:247], v133 offset:2048
	ds_read_b128 v[72:75], v127 offset:16
	ds_read_b128 v[76:79], v128 offset:16
	ds_read_b128 v[144:147], v127 offset:2064
	ds_read_b128 v[148:151], v128 offset:2064
	ds_read_b128 v[152:155], v127 offset:4112
	ds_read_b128 v[156:159], v128 offset:4112
	ds_read_b128 v[160:163], v127 offset:6160
	ds_read_b128 v[164:167], v128 offset:6160
	ds_read_b128 v[168:171], v127 offset:16400
	ds_read_b128 v[172:175], v128 offset:16400
	ds_read_b128 v[176:179], v127 offset:18448
	ds_read_b128 v[180:183], v128 offset:18448
	ds_read_b128 v[184:187], v127 offset:20496
	ds_read_b128 v[188:191], v128 offset:20496
	ds_read_b128 v[192:195], v127 offset:22544
	ds_read_b128 v[196:199], v128 offset:22544
	s_waitcnt lgkmcnt(0)
	s_cmp_ge_u32 s82, 14
	s_cbranch_scc1 .Lkl_m1npre_y_nd0
	s_lshl_b32 s77, s82, 7
	s_addk_i32 s77, 0x100
	s_add_i32 s78, s77, 0x20000
	s_add_i32 s79, s77, 0x2000
	s_add_i32 s80, s77, 0x22000
	s_mov_b32 m0, s23
	s_nop 0
	buffer_load_dwordx4 v122, s[4:7], s77 offen lds
	s_mov_b32 m0, s61
	s_nop 0
	buffer_load_dwordx4 v120, s[8:11], s77 offen lds
	s_mov_b32 m0, s39
	s_nop 0
	buffer_load_dwordx4 v122, s[4:7], s78 offen lds
	s_mov_b32 m0, s62
	s_nop 0
	buffer_load_dwordx4 v123, s[8:11], s77 offen lds
	s_mov_b32 m0, s63
	s_nop 0
	buffer_load_dwordx4 v122, s[4:7], s79 offen lds
	s_mov_b32 m0, s67
	s_nop 0
	buffer_load_dwordx4 v121, s[8:11], s77 offen lds
	s_mov_b32 m0, s66
	s_nop 0
	buffer_load_dwordx4 v122, s[4:7], s80 offen lds
	s_mov_b32 m0, s68
	s_nop 0
	buffer_load_dwordx4 v124, s[8:11], s77 offen lds
	s_waitcnt vmcnt(8)
	s_branch .Lkl_m1npre_y_nd0_j

; #define G_WAIT_V(n) asm volatile("s_waitcnt vmcnt(" #n ")" ::: "memory")
; #define G_BAR() __builtin_amdgcn_s_barrier()
; #define G_SCHED() __builtin_amdgcn_sched_barrier(0)
; #define D_STAGE_A(slot, half, kt) D_STAGE(rsA, voffA, slot, half, kt)
; #define D_STAGE_B(slot, half, kt) D_STAGE(rsB, voffB, slot, half, kt)
; #define D_LDA(dst, slot) do { _Pragma("unroll") for (int m = 0; m < 4; ++m) _Pragma("unroll") for (int k = 0; k < 2; ++k) \
;     dst[m][k] = *(const LDS_AS bf16x8*)(lds + (slot) + aoff + m * 2048 + k * 1024); } while (0)
; #define D_LDB(dst, slot) do { _Pragma("unroll") for (int n = 0; n < 2; ++n) _Pragma("unroll") for (int k = 0; k < 2; ++k) \
;     dst[n][k] = *(const LDS_AS bf16x8*)(lds + (slot) + boff + n * 2048 + k * 1024); } while (0)
; #define D_MMA(ai, bj, At, Bf) do { __builtin_amdgcn_s_setprio(1); _Pragma("unroll") for (int m = 0; m < 4; ++m) _Pragma("unroll") for (int n = 0; n < 2; ++n) _Pragma("unroll") for (int k = 0; k < 2; ++k) \
;     acc[ai][bj][m][n] = __builtin_amdgcn_mfma_f32_16x16x32_bf16(Bf[n][k], At[m][k], acc[ai][bj][m][n], 0, 0, 0); __builtin_amdgcn_s_setprio(0); } while (0)
; #define D_WAIT_L(n) asm volatile("s_waitcnt lgkmcnt(" #n ")" ::: "memory")
;     ...
;     D_LDB(B0, G_SB(0, 0)); G_SCHED(); D_LDA(At, G_SA(0, 0)); D_STAGE_A(G_SA(1, 1), 1, t1);
;     D_WAIT_L(8); G_BAR(); D_WAIT_L(0); G_SCHED(); D_MMA(0, 0, At, B0); G_BAR(); G_SCHED();
;     D_LDB(B1, G_SB(0, 1)); D_STAGE_B(G_SB(0, 0), 0, t2);
;     G_BAR(); D_WAIT_L(0); G_SCHED(); D_MMA(0, 1, At, B1); G_BAR(); G_SCHED();
;     D_LDA(At, G_SA(0, 1)); D_STAGE_A(G_SA(0, 0), 0, t2);
;     G_BAR(); D_WAIT_L(0); G_SCHED(); D_MMA(1, 0, At, B0); G_BAR(); G_SCHED();
;     D_STAGE_B(G_SB(0, 1), 1, t2);
;     G_WAIT_V(6); G_BAR(); G_SCHED(); D_MMA(1, 1, At, B1); G_BAR(); G_SCHED();
;     D_LDB(B0, G_SB(1, 0)); G_SCHED(); D_LDA(At, G_SA(1, 0)); D_STAGE_A(G_SA(0, 1), 1, t2);
;     D_WAIT_L(8); G_BAR(); D_WAIT_L(0); G_SCHED(); D_MMA(0, 0, At, B0); G_BAR(); G_SCHED();
;     D_LDB(B1, G_SB(1, 1)); D_STAGE_B(G_SB(1, 0), 0, t3);
;     G_BAR(); D_WAIT_L(0); G_SCHED(); D_MMA(0, 1, At, B1); G_BAR(); G_SCHED();
;     D_LDA(At, G_SA(1, 1)); D_STAGE_A(G_SA(1, 0), 0, t3);
;     G_BAR(); D_WAIT_L(0); G_SCHED(); D_MMA(1, 0, At, B0); G_BAR(); G_SCHED();
;     D_STAGE_B(G_SB(1, 1), 1, t3);
;     G_WAIT_V(6); G_BAR(); G_SCHED(); D_MMA(1, 1, At, B1); G_BAR(); G_SCHED();
.Lkl_m1npre_y_nd0_j:
	s_barrier
	s_setprio 1
	v_mfma_scale_f32_16x16x128_f8f6f4 v[140:143], v[200:207], v[72:79], v[140:143], v81, v80 op_sel_hi:[0,0,0]
	v_mfma_scale_f32_16x16x128_f8f6f4 v[136:139], v[220:227], v[72:79], v[136:139], v81, v80 op_sel_hi:[0,0,0]
	v_mfma_scale_f32_16x16x128_f8f6f4 v[108:111], v[200:207], v[144:151], v[108:111], v81, v80 op_sel_hi:[0,0,0]
	v_mfma_scale_f32_16x16x128_f8f6f4 v[104:107], v[220:227], v[144:151], v[104:107], v81, v80 op_sel_hi:[0,0,0]
	v_mfma_scale_f32_16x16x128_f8f6f4 v[92:95], v[200:207], v[152:159], v[92:95], v81, v80 op_sel_hi:[0,0,0]
	v_mfma_scale_f32_16x16x128_f8f6f4 v[88:91], v[220:227], v[152:159], v[88:91], v81, v80 op_sel_hi:[0,0,0]
	v_mfma_scale_f32_16x16x128_f8f6f4 v[212:215], v[200:207], v[160:167], v[212:215], v81, v80 op_sel_hi:[0,0,0]
	v_mfma_scale_f32_16x16x128_f8f6f4 v[216:219], v[220:227], v[160:167], v[216:219], v81, v80 op_sel_hi:[0,0,0]
	v_mfma_scale_f32_16x16x128_f8f6f4 v[116:119], v[228:235], v[72:79], v[116:119], v81, v80 op_sel_hi:[0,0,0]
	v_mfma_scale_f32_16x16x128_f8f6f4 v[112:115], v[240:247], v[72:79], v[112:115], v81, v80 op_sel_hi:[0,0,0]
	v_mfma_scale_f32_16x16x128_f8f6f4 v[100:103], v[228:235], v[144:151], v[100:103], v81, v80 op_sel_hi:[0,0,0]
	v_mfma_scale_f32_16x16x128_f8f6f4 v[96:99], v[240:247], v[144:151], v[96:99], v81, v80 op_sel_hi:[0,0,0]
	v_mfma_scale_f32_16x16x128_f8f6f4 v[84:87], v[228:235], v[152:159], v[84:87], v81, v80 op_sel_hi:[0,0,0]
	v_mfma_scale_f32_16x16x128_f8f6f4 v[8:11], v[240:247], v[152:159], v[8:11], v81, v80 op_sel_hi:[0,0,0]
	v_mfma_scale_f32_16x16x128_f8f6f4 v[68:71], v[228:235], v[160:167], v[68:71], v81, v80 op_sel_hi:[0,0,0]
	v_mfma_scale_f32_16x16x128_f8f6f4 v[56:59], v[240:247], v[160:167], v[56:59], v81, v80 op_sel_hi:[0,0,0]
	v_mfma_scale_f32_16x16x128_f8f6f4 v[64:67], v[200:207], v[168:175], v[64:67], v81, v80 op_sel_hi:[0,0,0]
	v_mfma_scale_f32_16x16x128_f8f6f4 v[60:63], v[220:227], v[168:175], v[60:63], v81, v80 op_sel_hi:[0,0,0]
	v_mfma_scale_f32_16x16x128_f8f6f4 v[44:47], v[200:207], v[176:183], v[44:47], v81, v80 op_sel_hi:[0,0,0]
	v_mfma_scale_f32_16x16x128_f8f6f4 v[40:43], v[220:227], v[176:183], v[40:43], v81, v80 op_sel_hi:[0,0,0]
	v_mfma_scale_f32_16x16x128_f8f6f4 v[28:31], v[200:207], v[184:191], v[28:31], v81, v80 op_sel_hi:[0,0,0]
	v_mfma_scale_f32_16x16x128_f8f6f4 v[24:27], v[220:227], v[184:191], v[24:27], v81, v80 op_sel_hi:[0,0,0]
	v_mfma_scale_f32_16x16x128_f8f6f4 v[12:15], v[200:207], v[192:199], v[12:15], v81, v80 op_sel_hi:[0,0,0]
	v_mfma_scale_f32_16x16x128_f8f6f4 v[236:239], v[220:227], v[192:199], v[236:239], v81, v80 op_sel_hi:[0,0,0]
	v_mfma_scale_f32_16x16x128_f8f6f4 v[52:55], v[228:235], v[168:175], v[52:55], v81, v80 op_sel_hi:[0,0,0]
	v_mfma_scale_f32_16x16x128_f8f6f4 v[48:51], v[240:247], v[168:175], v[48:51], v81, v80 op_sel_hi:[0,0,0]
	v_mfma_scale_f32_16x16x128_f8f6f4 v[36:39], v[228:235], v[176:183], v[36:39], v81, v80 op_sel_hi:[0,0,0]
	v_mfma_scale_f32_16x16x128_f8f6f4 v[32:35], v[240:247], v[176:183], v[32:35], v81, v80 op_sel_hi:[0,0,0]
	v_mfma_scale_f32_16x16x128_f8f6f4 v[20:23], v[228:235], v[184:191], v[20:23], v81, v80 op_sel_hi:[0,0,0]
	v_mfma_scale_f32_16x16x128_f8f6f4 v[16:19], v[240:247], v[184:191], v[16:19], v81, v80 op_sel_hi:[0,0,0]
	v_mfma_scale_f32_16x16x128_f8f6f4 v[4:7], v[228:235], v[192:199], v[4:7], v81, v80 op_sel_hi:[0,0,0]
	v_mfma_scale_f32_16x16x128_f8f6f4 v[0:3], v[240:247], v[192:199], v[0:3], v81, v80 op_sel_hi:[0,0,0]
	s_setprio 0
	s_barrier
	ds_read_b128 v[200:203], v134
	ds_read_b128 v[204:207], v135
	ds_read_b128 v[220:223], v134 offset:2048
	ds_read_b128 v[224:227], v135 offset:2048
	ds_read_b128 v[228:231], v208
	ds_read_b128 v[232:235], v209
	ds_read_b128 v[240:243], v208 offset:2048
	ds_read_b128 v[244:247], v209 offset:2048
	ds_read_b128 v[72:75], v127 offset:32784
	ds_read_b128 v[76:79], v128 offset:32784
	ds_read_b128 v[144:147], v127 offset:34832
	ds_read_b128 v[148:151], v128 offset:34832
	ds_read_b128 v[152:155], v127 offset:36880
	ds_read_b128 v[156:159], v128 offset:36880
	ds_read_b128 v[160:163], v127 offset:38928
	ds_read_b128 v[164:167], v128 offset:38928
	ds_read_b128 v[168:171], v127 offset:49168
	ds_read_b128 v[172:175], v128 offset:49168
	ds_read_b128 v[176:179], v127 offset:51216
	ds_read_b128 v[180:183], v128 offset:51216
	ds_read_b128 v[184:187], v127 offset:53264
	ds_read_b128 v[188:191], v128 offset:53264
	ds_read_b128 v[192:195], v127 offset:55312
	ds_read_b128 v[196:199], v128 offset:55312
	s_waitcnt lgkmcnt(0)
	s_cmp_ge_u32 s82, 14
	s_cbranch_scc1 .Lkl_m1npre_y_nd1
	s_lshl_b32 s77, s82, 7
	s_addk_i32 s77, 0x180
	s_add_i32 s78, s77, 0x20000
	s_add_i32 s79, s77, 0x2000
	s_add_i32 s80, s77, 0x22000
	s_mov_b32 m0, s69
	s_nop 0
	buffer_load_dwordx4 v122, s[4:7], s77 offen lds
	s_mov_b32 m0, s71
	s_nop 0
	buffer_load_dwordx4 v120, s[8:11], s77 offen lds
	s_mov_b32 m0, s70
	s_nop 0
	buffer_load_dwordx4 v122, s[4:7], s78 offen lds
	s_mov_b32 m0, s72
	s_nop 0
	buffer_load_dwordx4 v123, s[8:11], s77 offen lds
	s_mov_b32 m0, s73
	s_nop 0
	buffer_load_dwordx4 v122, s[4:7], s79 offen lds
	s_mov_b32 m0, s75
	s_nop 0
	buffer_load_dwordx4 v121, s[8:11], s77 offen lds
	s_mov_b32 m0, s74
	s_nop 0
	buffer_load_dwordx4 v122, s[4:7], s80 offen lds
	s_mov_b32 m0, s76
	s_nop 0
	buffer_load_dwordx4 v124, s[8:11], s77 offen lds
	s_waitcnt vmcnt(8)
	s_branch .Lkl_m1npre_y_nd1_j

; #define G_WAIT_V(n) asm volatile("s_waitcnt vmcnt(" #n ")" ::: "memory")
; #define G_BAR() __builtin_amdgcn_s_barrier()
; #define G_SCHED() __builtin_amdgcn_sched_barrier(0)
; #define D_STAGE_A(slot, half, kt) D_STAGE(rsA, voffA, slot, half, kt)
; #define D_STAGE_B(slot, half, kt) D_STAGE(rsB, voffB, slot, half, kt)
; #define D_LDA(dst, slot) do { _Pragma("unroll") for (int m = 0; m < 4; ++m) _Pragma("unroll") for (int k = 0; k < 2; ++k) \
;     dst[m][k] = *(const LDS_AS bf16x8*)(lds + (slot) + aoff + m * 2048 + k * 1024); } while (0)
; #define D_LDB(dst, slot) do { _Pragma("unroll") for (int n = 0; n < 2; ++n) _Pragma("unroll") for (int k = 0; k < 2; ++k) \
;     dst[n][k] = *(const LDS_AS bf16x8*)(lds + (slot) + boff + n * 2048 + k * 1024); } while (0)
; #define D_MMA(ai, bj, At, Bf) do { __builtin_amdgcn_s_setprio(1); _Pragma("unroll") for (int m = 0; m < 4; ++m) _Pragma("unroll") for (int n = 0; n < 2; ++n) _Pragma("unroll") for (int k = 0; k < 2; ++k) \
;     acc[ai][bj][m][n] = __builtin_amdgcn_mfma_f32_16x16x32_bf16(Bf[n][k], At[m][k], acc[ai][bj][m][n], 0, 0, 0); __builtin_amdgcn_s_setprio(0); } while (0)
; #define D_WAIT_L(n) asm volatile("s_waitcnt lgkmcnt(" #n ")" ::: "memory")
; #define D_STAGE_A(slot, half, kt) D_STAGE(rsA, voffA, slot, half, kt)
; #define D_STAGE_B(slot, half, kt) do { _Pragma("unroll") for (int _i = 0; _i < 2; ++_i) { const unsigned _m0 = ldsw + (unsigned)((slot) + _i * 8192); const unsigned _so = (unsigned)(kt) * 128u + (half) * bt_half + _i * bt_piece; \
;     asm volatile("s_mov_b32 m0, %0\n\ts_nop 4\n\tbuffer_load_dwordx4 %1, %2, %3 offen lds" :: "s"(_m0), "v"(voffB0), "s"(rsB), "s"(_so) : "m0", "memory"); } } while (0)
; #define D_WAIT_L(n) asm volatile("s_waitcnt lgkmcnt(" #n ")" ::: "memory")
;     ...
;     D_LDB(B0, G_SB(1, 0)); G_SCHED(); D_LDA(At, G_SA(1, 0)); D_STAGE_A(G_SA(0, 1), 1, t2);
;     D_WAIT_L(8); G_BAR(); D_WAIT_L(0); G_SCHED(); D_MMA(0, 0, At, B0); G_BAR(); G_SCHED();
;     D_LDB(B1, G_SB(1, 1)); D_STAGE_B(G_SB(1, 0), 0, t3);
;     G_BAR(); D_WAIT_L(0); G_SCHED(); D_MMA(0, 1, At, B1); G_BAR(); G_SCHED();
;     D_LDA(At, G_SA(1, 1)); D_STAGE_A(G_SA(1, 0), 0, t3);
;     G_BAR(); D_WAIT_L(0); G_SCHED(); D_MMA(1, 0, At, B0); G_BAR(); G_SCHED();
;     D_STAGE_B(G_SB(1, 1), 1, t3);
;     G_WAIT_V(6); G_BAR(); G_SCHED(); D_MMA(1, 1, At, B1); G_BAR(); G_SCHED();
;   }
.Lkl_m1npre_y_nd1_j:
	s_barrier
	s_setprio 1
	v_mfma_scale_f32_16x16x128_f8f6f4 v[140:143], v[200:207], v[72:79], v[140:143], v81, v80 op_sel_hi:[0,0,0]
	v_mfma_scale_f32_16x16x128_f8f6f4 v[136:139], v[220:227], v[72:79], v[136:139], v81, v80 op_sel_hi:[0,0,0]
	v_mfma_scale_f32_16x16x128_f8f6f4 v[108:111], v[200:207], v[144:151], v[108:111], v81, v80 op_sel_hi:[0,0,0]
	v_mfma_scale_f32_16x16x128_f8f6f4 v[104:107], v[220:227], v[144:151], v[104:107], v81, v80 op_sel_hi:[0,0,0]
	v_mfma_scale_f32_16x16x128_f8f6f4 v[92:95], v[200:207], v[152:159], v[92:95], v81, v80 op_sel_hi:[0,0,0]
	v_mfma_scale_f32_16x16x128_f8f6f4 v[88:91], v[220:227], v[152:159], v[88:91], v81, v80 op_sel_hi:[0,0,0]
	v_mfma_scale_f32_16x16x128_f8f6f4 v[212:215], v[200:207], v[160:167], v[212:215], v81, v80 op_sel_hi:[0,0,0]
	v_mfma_scale_f32_16x16x128_f8f6f4 v[216:219], v[220:227], v[160:167], v[216:219], v81, v80 op_sel_hi:[0,0,0]
	v_mfma_scale_f32_16x16x128_f8f6f4 v[116:119], v[228:235], v[72:79], v[116:119], v81, v80 op_sel_hi:[0,0,0]
	v_mfma_scale_f32_16x16x128_f8f6f4 v[112:115], v[240:247], v[72:79], v[112:115], v81, v80 op_sel_hi:[0,0,0]
	v_mfma_scale_f32_16x16x128_f8f6f4 v[100:103], v[228:235], v[144:151], v[100:103], v81, v80 op_sel_hi:[0,0,0]
	v_mfma_scale_f32_16x16x128_f8f6f4 v[96:99], v[240:247], v[144:151], v[96:99], v81, v80 op_sel_hi:[0,0,0]
	v_mfma_scale_f32_16x16x128_f8f6f4 v[84:87], v[228:235], v[152:159], v[84:87], v81, v80 op_sel_hi:[0,0,0]
	v_mfma_scale_f32_16x16x128_f8f6f4 v[8:11], v[240:247], v[152:159], v[8:11], v81, v80 op_sel_hi:[0,0,0]
	v_mfma_scale_f32_16x16x128_f8f6f4 v[68:71], v[228:235], v[160:167], v[68:71], v81, v80 op_sel_hi:[0,0,0]
	v_mfma_scale_f32_16x16x128_f8f6f4 v[56:59], v[240:247], v[160:167], v[56:59], v81, v80 op_sel_hi:[0,0,0]
	v_mfma_scale_f32_16x16x128_f8f6f4 v[64:67], v[200:207], v[168:175], v[64:67], v81, v80 op_sel_hi:[0,0,0]
	v_mfma_scale_f32_16x16x128_f8f6f4 v[60:63], v[220:227], v[168:175], v[60:63], v81, v80 op_sel_hi:[0,0,0]
	v_mfma_scale_f32_16x16x128_f8f6f4 v[44:47], v[200:207], v[176:183], v[44:47], v81, v80 op_sel_hi:[0,0,0]
	v_mfma_scale_f32_16x16x128_f8f6f4 v[40:43], v[220:227], v[176:183], v[40:43], v81, v80 op_sel_hi:[0,0,0]
	v_mfma_scale_f32_16x16x128_f8f6f4 v[28:31], v[200:207], v[184:191], v[28:31], v81, v80 op_sel_hi:[0,0,0]
	v_mfma_scale_f32_16x16x128_f8f6f4 v[24:27], v[220:227], v[184:191], v[24:27], v81, v80 op_sel_hi:[0,0,0]
	v_mfma_scale_f32_16x16x128_f8f6f4 v[12:15], v[200:207], v[192:199], v[12:15], v81, v80 op_sel_hi:[0,0,0]
	v_mfma_scale_f32_16x16x128_f8f6f4 v[236:239], v[220:227], v[192:199], v[236:239], v81, v80 op_sel_hi:[0,0,0]
	v_mfma_scale_f32_16x16x128_f8f6f4 v[52:55], v[228:235], v[168:175], v[52:55], v81, v80 op_sel_hi:[0,0,0]
	v_mfma_scale_f32_16x16x128_f8f6f4 v[48:51], v[240:247], v[168:175], v[48:51], v81, v80 op_sel_hi:[0,0,0]
	v_mfma_scale_f32_16x16x128_f8f6f4 v[36:39], v[228:235], v[176:183], v[36:39], v81, v80 op_sel_hi:[0,0,0]
	v_mfma_scale_f32_16x16x128_f8f6f4 v[32:35], v[240:247], v[176:183], v[32:35], v81, v80 op_sel_hi:[0,0,0]
	v_mfma_scale_f32_16x16x128_f8f6f4 v[20:23], v[228:235], v[184:191], v[20:23], v81, v80 op_sel_hi:[0,0,0]
	v_mfma_scale_f32_16x16x128_f8f6f4 v[16:19], v[240:247], v[184:191], v[16:19], v81, v80 op_sel_hi:[0,0,0]
	v_mfma_scale_f32_16x16x128_f8f6f4 v[4:7], v[228:235], v[192:199], v[4:7], v81, v80 op_sel_hi:[0,0,0]
	v_mfma_scale_f32_16x16x128_f8f6f4 v[0:3], v[240:247], v[192:199], v[0:3], v81, v80 op_sel_hi:[0,0,0]
	s_setprio 0
	s_barrier
	s_add_i32 s82, s82, 2
	s_cmp_lt_u32 s82, 16
	s_cbranch_scc1 .Lkl_m1npre_yl

; #define G_WAIT_V(n) asm volatile("s_waitcnt vmcnt(" #n ")" ::: "memory")
; #define G_BAR() __builtin_amdgcn_s_barrier()
; #define G_SCHED() __builtin_amdgcn_sched_barrier(0)
; #define D_STAGE_A(slot, half, kt) D_STAGE(rsA, voffA, slot, half, kt)
; #define D_STAGE_B(slot, half, kt) D_STAGE(rsB, voffB, slot, half, kt)
; #define D_LDA(dst, slot) do { _Pragma("unroll") for (int m = 0; m < 4; ++m) _Pragma("unroll") for (int k = 0; k < 2; ++k) \
;     dst[m][k] = *(const LDS_AS bf16x8*)(lds + (slot) + aoff + m * 2048 + k * 1024); } while (0)
; #define D_LDB(dst, slot) do { _Pragma("unroll") for (int n = 0; n < 2; ++n) _Pragma("unroll") for (int k = 0; k < 2; ++k) \
;     dst[n][k] = *(const LDS_AS bf16x8*)(lds + (slot) + boff + n * 2048 + k * 1024); } while (0)
; #define D_MMA(ai, bj, At, Bf) do { __builtin_amdgcn_s_setprio(1); _Pragma("unroll") for (int m = 0; m < 4; ++m) _Pragma("unroll") for (int n = 0; n < 2; ++n) _Pragma("unroll") for (int k = 0; k < 2; ++k) \
;     acc[ai][bj][m][n] = __builtin_amdgcn_mfma_f32_16x16x32_bf16(Bf[n][k], At[m][k], acc[ai][bj][m][n], 0, 0, 0); __builtin_amdgcn_s_setprio(0); } while (0)
; #define D_WAIT_L(n) asm volatile("s_waitcnt lgkmcnt(" #n ")" ::: "memory")
; #define D_STAGE_A(slot, half, kt) D_STAGE(rsA, voffA, slot, half, kt)
; #define D_STAGE_B(slot, half, kt) do { _Pragma("unroll") for (int _i = 0; _i < 2; ++_i) { const unsigned _m0 = ldsw + (unsigned)((slot) + _i * 8192); const unsigned _so = (unsigned)(kt) * 128u + (half) * bt_half + _i * bt_piece; \
;     asm volatile("s_mov_b32 m0, %0\n\ts_nop 4\n\tbuffer_load_dwordx4 %1, %2, %3 offen lds" :: "s"(_m0), "v"(voffB0), "s"(rsB), "s"(_so) : "m0", "memory"); } } while (0)
; #define D_WAIT_L(n) asm volatile("s_waitcnt lgkmcnt(" #n ")" ::: "memory")
;     ...
;     D_LDB(B0, G_SB(0, 0)); G_SCHED(); D_LDA(At, G_SA(0, 0)); D_STAGE_A(G_SA(1, 1), 1, t1);
;     D_WAIT_L(8); G_BAR(); D_WAIT_L(0); G_SCHED(); D_MMA(0, 0, At, B0); G_BAR(); G_SCHED();
;     D_LDB(B1, G_SB(0, 1)); D_STAGE_B(G_SB(0, 0), 0, t2);
;     G_BAR(); D_WAIT_L(0); G_SCHED(); D_MMA(0, 1, At, B1); G_BAR(); G_SCHED();
;     D_LDA(At, G_SA(0, 1)); D_STAGE_A(G_SA(0, 0), 0, t2);
;     G_BAR(); D_WAIT_L(0); G_SCHED(); D_MMA(1, 0, At, B0); G_BAR(); G_SCHED();
;     D_STAGE_B(G_SB(0, 1), 1, t2);
;     G_WAIT_V(6); G_BAR(); G_SCHED(); D_MMA(1, 1, At, B1); G_BAR(); G_SCHED();
.Lkl_m1pre_yl:
	ds_read_b128 v[200:203], v130
	ds_read_b128 v[204:207], v131
	ds_read_b128 v[208:211], v130 offset:2048
	ds_read_b128 v[212:215], v131 offset:2048
	ds_read_b128 v[228:231], v132
	ds_read_b128 v[232:235], v133
	ds_read_b128 v[236:239], v132 offset:2048
	ds_read_b128 v[240:243], v133 offset:2048
	ds_read_b128 v[72:75], v127 offset:16
	ds_read_b128 v[76:79], v128 offset:16
	ds_read_b128 v[144:147], v127 offset:2064
	ds_read_b128 v[148:151], v128 offset:2064
	ds_read_b128 v[152:155], v127 offset:4112
	ds_read_b128 v[156:159], v128 offset:4112
	ds_read_b128 v[160:163], v127 offset:6160
	ds_read_b128 v[164:167], v128 offset:6160
	ds_read_b128 v[168:171], v127 offset:16400
	ds_read_b128 v[172:175], v128 offset:16400
	ds_read_b128 v[176:179], v127 offset:18448
	ds_read_b128 v[180:183], v128 offset:18448
	ds_read_b128 v[184:187], v127 offset:20496
	ds_read_b128 v[188:191], v128 offset:20496
	ds_read_b128 v[192:195], v127 offset:22544
	ds_read_b128 v[196:199], v128 offset:22544
	s_waitcnt lgkmcnt(0)
	s_cmp_ge_u32 s77, 14
	s_cbranch_scc1 .Lkl_m1pre_y_nd0
	s_lshl_b32 s72, s77, 7
	s_addk_i32 s72, 0x100
	s_add_i32 s73, s72, 0x20000
	s_add_i32 s74, s72, 0x2000
	s_add_i32 s75, s72, 0x22000
	s_mov_b32 m0, s27
	s_nop 0
	buffer_load_dwordx4 v126, s[4:7], s72 offen lds
	s_mov_b32 m0, s17
	s_nop 0
	buffer_load_dwordx4 v120, s[8:11], s72 offen lds
	s_mov_b32 m0, s63
	s_nop 0
	buffer_load_dwordx4 v126, s[4:7], s73 offen lds
	s_mov_b32 m0, s66
	s_nop 0
	buffer_load_dwordx4 v121, s[8:11], s72 offen lds
	s_mov_b32 m0, s28
	s_nop 0
	buffer_load_dwordx4 v126, s[4:7], s74 offen lds
	s_mov_b32 m0, s29
	s_nop 0
	buffer_load_dwordx4 v122, s[8:11], s72 offen lds
	s_mov_b32 m0, s67
	s_nop 0
	buffer_load_dwordx4 v126, s[4:7], s75 offen lds
	s_mov_b32 m0, s68
	s_nop 0
	buffer_load_dwordx4 v123, s[8:11], s72 offen lds
	s_waitcnt vmcnt(8)
	s_branch .Lkl_m1pre_y_nd0_j

; #define G_WAIT_V(n) asm volatile("s_waitcnt vmcnt(" #n ")" ::: "memory")
; #define G_BAR() __builtin_amdgcn_s_barrier()
; #define G_SCHED() __builtin_amdgcn_sched_barrier(0)
; #define D_STAGE_A(slot, half, kt) D_STAGE(rsA, voffA, slot, half, kt)
; #define D_STAGE_B(slot, half, kt) D_STAGE(rsB, voffB, slot, half, kt)
; #define D_LDA(dst, slot) do { _Pragma("unroll") for (int m = 0; m < 4; ++m) _Pragma("unroll") for (int k = 0; k < 2; ++k) \
;     dst[m][k] = *(const LDS_AS bf16x8*)(lds + (slot) + aoff + m * 2048 + k * 1024); } while (0)
; #define D_LDB(dst, slot) do { _Pragma("unroll") for (int n = 0; n < 2; ++n) _Pragma("unroll") for (int k = 0; k < 2; ++k) \
;     dst[n][k] = *(const LDS_AS bf16x8*)(lds + (slot) + boff + n * 2048 + k * 1024); } while (0)
; #define D_MMA(ai, bj, At, Bf) do { __builtin_amdgcn_s_setprio(1); _Pragma("unroll") for (int m = 0; m < 4; ++m) _Pragma("unroll") for (int n = 0; n < 2; ++n) _Pragma("unroll") for (int k = 0; k < 2; ++k) \
;     acc[ai][bj][m][n] = __builtin_amdgcn_mfma_f32_16x16x32_bf16(Bf[n][k], At[m][k], acc[ai][bj][m][n], 0, 0, 0); __builtin_amdgcn_s_setprio(0); } while (0)
; #define D_WAIT_L(n) asm volatile("s_waitcnt lgkmcnt(" #n ")" ::: "memory")
;     ...
;     D_LDB(B0, G_SB(0, 0)); G_SCHED(); D_LDA(At, G_SA(0, 0)); D_STAGE_A(G_SA(1, 1), 1, t1);
;     D_WAIT_L(8); G_BAR(); D_WAIT_L(0); G_SCHED(); D_MMA(0, 0, At, B0); G_BAR(); G_SCHED();
;     D_LDB(B1, G_SB(0, 1)); D_STAGE_B(G_SB(0, 0), 0, t2);
;     G_BAR(); D_WAIT_L(0); G_SCHED(); D_MMA(0, 1, At, B1); G_BAR(); G_SCHED();
;     D_LDA(At, G_SA(0, 1)); D_STAGE_A(G_SA(0, 0), 0, t2);
;     G_BAR(); D_WAIT_L(0); G_SCHED(); D_MMA(1, 0, At, B0); G_BAR(); G_SCHED();
;     D_STAGE_B(G_SB(0, 1), 1, t2);
;     G_WAIT_V(6); G_BAR(); G_SCHED(); D_MMA(1, 1, At, B1); G_BAR(); G_SCHED();
;     D_LDB(B0, G_SB(1, 0)); G_SCHED(); D_LDA(At, G_SA(1, 0)); D_STAGE_A(G_SA(0, 1), 1, t2);
;     D_WAIT_L(8); G_BAR(); D_WAIT_L(0); G_SCHED(); D_MMA(0, 0, At, B0); G_BAR(); G_SCHED();
;     D_LDB(B1, G_SB(1, 1)); D_STAGE_B(G_SB(1, 0), 0, t3);
;     G_BAR(); D_WAIT_L(0); G_SCHED(); D_MMA(0, 1, At, B1); G_BAR(); G_SCHED();
;     D_LDA(At, G_SA(1, 1)); D_STAGE_A(G_SA(1, 0), 0, t3);
;     G_BAR(); D_WAIT_L(0); G_SCHED(); D_MMA(1, 0, At, B0); G_BAR(); G_SCHED();
;     D_STAGE_B(G_SB(1, 1), 1, t3);
;     G_WAIT_V(6); G_BAR(); G_SCHED(); D_MMA(1, 1, At, B1); G_BAR(); G_SCHED();
.Lkl_m1pre_y_nd0_j:
	s_barrier
	s_setprio 1
	v_mfma_scale_f32_16x16x128_f8f6f4 v[140:143], v[200:207], v[72:79], v[140:143], v81, v80 op_sel_hi:[0,0,0]
	v_mfma_scale_f32_16x16x128_f8f6f4 v[136:139], v[208:215], v[72:79], v[136:139], v81, v80 op_sel_hi:[0,0,0]
	v_mfma_scale_f32_16x16x128_f8f6f4 v[108:111], v[200:207], v[144:151], v[108:111], v81, v80 op_sel_hi:[0,0,0]
	v_mfma_scale_f32_16x16x128_f8f6f4 v[104:107], v[208:215], v[144:151], v[104:107], v81, v80 op_sel_hi:[0,0,0]
	v_mfma_scale_f32_16x16x128_f8f6f4 v[92:95], v[200:207], v[152:159], v[92:95], v81, v80 op_sel_hi:[0,0,0]
	v_mfma_scale_f32_16x16x128_f8f6f4 v[88:91], v[208:215], v[152:159], v[88:91], v81, v80 op_sel_hi:[0,0,0]
	v_mfma_scale_f32_16x16x128_f8f6f4 v[220:223], v[200:207], v[160:167], v[220:223], v81, v80 op_sel_hi:[0,0,0]
	v_mfma_scale_f32_16x16x128_f8f6f4 v[224:227], v[208:215], v[160:167], v[224:227], v81, v80 op_sel_hi:[0,0,0]
	v_mfma_scale_f32_16x16x128_f8f6f4 v[116:119], v[228:235], v[72:79], v[116:119], v81, v80 op_sel_hi:[0,0,0]
	v_mfma_scale_f32_16x16x128_f8f6f4 v[112:115], v[236:243], v[72:79], v[112:115], v81, v80 op_sel_hi:[0,0,0]
	v_mfma_scale_f32_16x16x128_f8f6f4 v[100:103], v[228:235], v[144:151], v[100:103], v81, v80 op_sel_hi:[0,0,0]
	v_mfma_scale_f32_16x16x128_f8f6f4 v[96:99], v[236:243], v[144:151], v[96:99], v81, v80 op_sel_hi:[0,0,0]
	v_mfma_scale_f32_16x16x128_f8f6f4 v[84:87], v[228:235], v[152:159], v[84:87], v81, v80 op_sel_hi:[0,0,0]
	v_mfma_scale_f32_16x16x128_f8f6f4 v[8:11], v[236:243], v[152:159], v[8:11], v81, v80 op_sel_hi:[0,0,0]
	v_mfma_scale_f32_16x16x128_f8f6f4 v[68:71], v[228:235], v[160:167], v[68:71], v81, v80 op_sel_hi:[0,0,0]
	v_mfma_scale_f32_16x16x128_f8f6f4 v[56:59], v[236:243], v[160:167], v[56:59], v81, v80 op_sel_hi:[0,0,0]
	v_mfma_scale_f32_16x16x128_f8f6f4 v[64:67], v[200:207], v[168:175], v[64:67], v81, v80 op_sel_hi:[0,0,0]
	v_mfma_scale_f32_16x16x128_f8f6f4 v[60:63], v[208:215], v[168:175], v[60:63], v81, v80 op_sel_hi:[0,0,0]
	v_mfma_scale_f32_16x16x128_f8f6f4 v[44:47], v[200:207], v[176:183], v[44:47], v81, v80 op_sel_hi:[0,0,0]
	v_mfma_scale_f32_16x16x128_f8f6f4 v[40:43], v[208:215], v[176:183], v[40:43], v81, v80 op_sel_hi:[0,0,0]
	v_mfma_scale_f32_16x16x128_f8f6f4 v[28:31], v[200:207], v[184:191], v[28:31], v81, v80 op_sel_hi:[0,0,0]
	v_mfma_scale_f32_16x16x128_f8f6f4 v[24:27], v[208:215], v[184:191], v[24:27], v81, v80 op_sel_hi:[0,0,0]
	v_mfma_scale_f32_16x16x128_f8f6f4 v[12:15], v[200:207], v[192:199], v[12:15], v81, v80 op_sel_hi:[0,0,0]
	v_mfma_scale_f32_16x16x128_f8f6f4 v[244:247], v[208:215], v[192:199], v[244:247], v81, v80 op_sel_hi:[0,0,0]
	v_mfma_scale_f32_16x16x128_f8f6f4 v[52:55], v[228:235], v[168:175], v[52:55], v81, v80 op_sel_hi:[0,0,0]
	v_mfma_scale_f32_16x16x128_f8f6f4 v[48:51], v[236:243], v[168:175], v[48:51], v81, v80 op_sel_hi:[0,0,0]
	v_mfma_scale_f32_16x16x128_f8f6f4 v[36:39], v[228:235], v[176:183], v[36:39], v81, v80 op_sel_hi:[0,0,0]
	v_mfma_scale_f32_16x16x128_f8f6f4 v[32:35], v[236:243], v[176:183], v[32:35], v81, v80 op_sel_hi:[0,0,0]
	v_mfma_scale_f32_16x16x128_f8f6f4 v[20:23], v[228:235], v[184:191], v[20:23], v81, v80 op_sel_hi:[0,0,0]
	v_mfma_scale_f32_16x16x128_f8f6f4 v[16:19], v[236:243], v[184:191], v[16:19], v81, v80 op_sel_hi:[0,0,0]
	v_mfma_scale_f32_16x16x128_f8f6f4 v[4:7], v[228:235], v[192:199], v[4:7], v81, v80 op_sel_hi:[0,0,0]
	v_mfma_scale_f32_16x16x128_f8f6f4 v[0:3], v[236:243], v[192:199], v[0:3], v81, v80 op_sel_hi:[0,0,0]
	s_setprio 0
	s_barrier
	ds_read_b128 v[200:203], v134
	ds_read_b128 v[204:207], v135
	ds_read_b128 v[208:211], v134 offset:2048
	ds_read_b128 v[212:215], v135 offset:2048
	ds_read_b128 v[228:231], v216
	ds_read_b128 v[232:235], v217
	ds_read_b128 v[236:239], v216 offset:2048
	ds_read_b128 v[240:243], v217 offset:2048
	ds_read_b128 v[72:75], v127 offset:32784
	ds_read_b128 v[76:79], v128 offset:32784
	ds_read_b128 v[144:147], v127 offset:34832
	ds_read_b128 v[148:151], v128 offset:34832
	ds_read_b128 v[152:155], v127 offset:36880
	ds_read_b128 v[156:159], v128 offset:36880
	ds_read_b128 v[160:163], v127 offset:38928
	ds_read_b128 v[164:167], v128 offset:38928
	ds_read_b128 v[168:171], v127 offset:49168
	ds_read_b128 v[172:175], v128 offset:49168
	ds_read_b128 v[176:179], v127 offset:51216
	ds_read_b128 v[180:183], v128 offset:51216
	ds_read_b128 v[184:187], v127 offset:53264
	ds_read_b128 v[188:191], v128 offset:53264
	ds_read_b128 v[192:195], v127 offset:55312
	ds_read_b128 v[196:199], v128 offset:55312
	s_waitcnt lgkmcnt(0)
	s_cmp_ge_u32 s77, 14
	s_cbranch_scc1 .Lkl_m1pre_y_nd1
	s_lshl_b32 s72, s77, 7
	s_addk_i32 s72, 0x180
	s_add_i32 s73, s72, 0x20000
	s_add_i32 s74, s72, 0x2000
	s_add_i32 s75, s72, 0x22000
	s_mov_b32 m0, s39
	s_nop 0
	buffer_load_dwordx4 v126, s[4:7], s72 offen lds
	s_mov_b32 m0, s60
	s_nop 0
	buffer_load_dwordx4 v120, s[8:11], s72 offen lds
	s_mov_b32 m0, s69
	s_nop 0
	buffer_load_dwordx4 v126, s[4:7], s73 offen lds
	s_mov_b32 m0, s70
	s_nop 0
	buffer_load_dwordx4 v121, s[8:11], s72 offen lds
	s_mov_b32 m0, s61
	s_nop 0
	buffer_load_dwordx4 v126, s[4:7], s74 offen lds
	s_mov_b32 m0, s26
	s_nop 0
	buffer_load_dwordx4 v122, s[8:11], s72 offen lds
	s_mov_b32 m0, s71
	s_nop 0
	buffer_load_dwordx4 v126, s[4:7], s75 offen lds
	s_mov_b32 m0, s62
	s_nop 0
	buffer_load_dwordx4 v123, s[8:11], s72 offen lds
	s_waitcnt vmcnt(8)
	s_branch .Lkl_m1pre_y_nd1_j

; #define G_WAIT_V(n) asm volatile("s_waitcnt vmcnt(" #n ")" ::: "memory")
; #define G_BAR() __builtin_amdgcn_s_barrier()
; #define G_SCHED() __builtin_amdgcn_sched_barrier(0)
; #define D_STAGE_A(slot, half, kt) D_STAGE(rsA, voffA, slot, half, kt)
; #define D_STAGE_B(slot, half, kt) D_STAGE(rsB, voffB, slot, half, kt)
; #define D_LDA(dst, slot) do { _Pragma("unroll") for (int m = 0; m < 4; ++m) _Pragma("unroll") for (int k = 0; k < 2; ++k) \
;     dst[m][k] = *(const LDS_AS bf16x8*)(lds + (slot) + aoff + m * 2048 + k * 1024); } while (0)
; #define D_LDB(dst, slot) do { _Pragma("unroll") for (int n = 0; n < 2; ++n) _Pragma("unroll") for (int k = 0; k < 2; ++k) \
;     dst[n][k] = *(const LDS_AS bf16x8*)(lds + (slot) + boff + n * 2048 + k * 1024); } while (0)
; #define D_MMA(ai, bj, At, Bf) do { __builtin_amdgcn_s_setprio(1); _Pragma("unroll") for (int m = 0; m < 4; ++m) _Pragma("unroll") for (int n = 0; n < 2; ++n) _Pragma("unroll") for (int k = 0; k < 2; ++k) \
;     acc[ai][bj][m][n] = __builtin_amdgcn_mfma_f32_16x16x32_bf16(Bf[n][k], At[m][k], acc[ai][bj][m][n], 0, 0, 0); __builtin_amdgcn_s_setprio(0); } while (0)
; #define D_WAIT_L(n) asm volatile("s_waitcnt lgkmcnt(" #n ")" ::: "memory")
; #define D_STAGE_A(slot, half, kt) D_STAGE(rsA, voffA, slot, half, kt)
; #define D_STAGE_B(slot, half, kt) do { _Pragma("unroll") for (int _i = 0; _i < 2; ++_i) { const unsigned _m0 = ldsw + (unsigned)((slot) + _i * 8192); const unsigned _so = (unsigned)(kt) * 128u + (half) * bt_half + _i * bt_piece; \
;     asm volatile("s_mov_b32 m0, %0\n\ts_nop 4\n\tbuffer_load_dwordx4 %1, %2, %3 offen lds" :: "s"(_m0), "v"(voffB0), "s"(rsB), "s"(_so) : "m0", "memory"); } } while (0)
; #define D_WAIT_L(n) asm volatile("s_waitcnt lgkmcnt(" #n ")" ::: "memory")
;     ...
;     D_LDB(B0, G_SB(1, 0)); G_SCHED(); D_LDA(At, G_SA(1, 0)); D_STAGE_A(G_SA(0, 1), 1, t2);
;     D_WAIT_L(8); G_BAR(); D_WAIT_L(0); G_SCHED(); D_MMA(0, 0, At, B0); G_BAR(); G_SCHED();
;     D_LDB(B1, G_SB(1, 1)); D_STAGE_B(G_SB(1, 0), 0, t3);
;     G_BAR(); D_WAIT_L(0); G_SCHED(); D_MMA(0, 1, At, B1); G_BAR(); G_SCHED();
;     D_LDA(At, G_SA(1, 1)); D_STAGE_A(G_SA(1, 0), 0, t3);
;     G_BAR(); D_WAIT_L(0); G_SCHED(); D_MMA(1, 0, At, B0); G_BAR(); G_SCHED();
;     D_STAGE_B(G_SB(1, 1), 1, t3);
;     G_WAIT_V(6); G_BAR(); G_SCHED(); D_MMA(1, 1, At, B1); G_BAR(); G_SCHED();
;   }
.Lkl_m1pre_y_nd1_j:
	s_barrier
	s_setprio 1
	v_mfma_scale_f32_16x16x128_f8f6f4 v[140:143], v[200:207], v[72:79], v[140:143], v81, v80 op_sel_hi:[0,0,0]
	v_mfma_scale_f32_16x16x128_f8f6f4 v[136:139], v[208:215], v[72:79], v[136:139], v81, v80 op_sel_hi:[0,0,0]
	v_mfma_scale_f32_16x16x128_f8f6f4 v[108:111], v[200:207], v[144:151], v[108:111], v81, v80 op_sel_hi:[0,0,0]
	v_mfma_scale_f32_16x16x128_f8f6f4 v[104:107], v[208:215], v[144:151], v[104:107], v81, v80 op_sel_hi:[0,0,0]
	v_mfma_scale_f32_16x16x128_f8f6f4 v[92:95], v[200:207], v[152:159], v[92:95], v81, v80 op_sel_hi:[0,0,0]
	v_mfma_scale_f32_16x16x128_f8f6f4 v[88:91], v[208:215], v[152:159], v[88:91], v81, v80 op_sel_hi:[0,0,0]
	v_mfma_scale_f32_16x16x128_f8f6f4 v[220:223], v[200:207], v[160:167], v[220:223], v81, v80 op_sel_hi:[0,0,0]
	v_mfma_scale_f32_16x16x128_f8f6f4 v[224:227], v[208:215], v[160:167], v[224:227], v81, v80 op_sel_hi:[0,0,0]
	v_mfma_scale_f32_16x16x128_f8f6f4 v[116:119], v[228:235], v[72:79], v[116:119], v81, v80 op_sel_hi:[0,0,0]
	v_mfma_scale_f32_16x16x128_f8f6f4 v[112:115], v[236:243], v[72:79], v[112:115], v81, v80 op_sel_hi:[0,0,0]
	v_mfma_scale_f32_16x16x128_f8f6f4 v[100:103], v[228:235], v[144:151], v[100:103], v81, v80 op_sel_hi:[0,0,0]
	v_mfma_scale_f32_16x16x128_f8f6f4 v[96:99], v[236:243], v[144:151], v[96:99], v81, v80 op_sel_hi:[0,0,0]
	v_mfma_scale_f32_16x16x128_f8f6f4 v[84:87], v[228:235], v[152:159], v[84:87], v81, v80 op_sel_hi:[0,0,0]
	v_mfma_scale_f32_16x16x128_f8f6f4 v[8:11], v[236:243], v[152:159], v[8:11], v81, v80 op_sel_hi:[0,0,0]
	v_mfma_scale_f32_16x16x128_f8f6f4 v[68:71], v[228:235], v[160:167], v[68:71], v81, v80 op_sel_hi:[0,0,0]
	v_mfma_scale_f32_16x16x128_f8f6f4 v[56:59], v[236:243], v[160:167], v[56:59], v81, v80 op_sel_hi:[0,0,0]
	v_mfma_scale_f32_16x16x128_f8f6f4 v[64:67], v[200:207], v[168:175], v[64:67], v81, v80 op_sel_hi:[0,0,0]
	v_mfma_scale_f32_16x16x128_f8f6f4 v[60:63], v[208:215], v[168:175], v[60:63], v81, v80 op_sel_hi:[0,0,0]
	v_mfma_scale_f32_16x16x128_f8f6f4 v[44:47], v[200:207], v[176:183], v[44:47], v81, v80 op_sel_hi:[0,0,0]
	v_mfma_scale_f32_16x16x128_f8f6f4 v[40:43], v[208:215], v[176:183], v[40:43], v81, v80 op_sel_hi:[0,0,0]
	v_mfma_scale_f32_16x16x128_f8f6f4 v[28:31], v[200:207], v[184:191], v[28:31], v81, v80 op_sel_hi:[0,0,0]
	v_mfma_scale_f32_16x16x128_f8f6f4 v[24:27], v[208:215], v[184:191], v[24:27], v81, v80 op_sel_hi:[0,0,0]
	v_mfma_scale_f32_16x16x128_f8f6f4 v[12:15], v[200:207], v[192:199], v[12:15], v81, v80 op_sel_hi:[0,0,0]
	v_mfma_scale_f32_16x16x128_f8f6f4 v[244:247], v[208:215], v[192:199], v[244:247], v81, v80 op_sel_hi:[0,0,0]
	v_mfma_scale_f32_16x16x128_f8f6f4 v[52:55], v[228:235], v[168:175], v[52:55], v81, v80 op_sel_hi:[0,0,0]
	v_mfma_scale_f32_16x16x128_f8f6f4 v[48:51], v[236:243], v[168:175], v[48:51], v81, v80 op_sel_hi:[0,0,0]
	v_mfma_scale_f32_16x16x128_f8f6f4 v[36:39], v[228:235], v[176:183], v[36:39], v81, v80 op_sel_hi:[0,0,0]
	v_mfma_scale_f32_16x16x128_f8f6f4 v[32:35], v[236:243], v[176:183], v[32:35], v81, v80 op_sel_hi:[0,0,0]
	v_mfma_scale_f32_16x16x128_f8f6f4 v[20:23], v[228:235], v[184:191], v[20:23], v81, v80 op_sel_hi:[0,0,0]
	v_mfma_scale_f32_16x16x128_f8f6f4 v[16:19], v[236:243], v[184:191], v[16:19], v81, v80 op_sel_hi:[0,0,0]
	v_mfma_scale_f32_16x16x128_f8f6f4 v[4:7], v[228:235], v[192:199], v[4:7], v81, v80 op_sel_hi:[0,0,0]
	v_mfma_scale_f32_16x16x128_f8f6f4 v[0:3], v[236:243], v[192:199], v[0:3], v81, v80 op_sel_hi:[0,0,0]
	s_setprio 0
	s_barrier
	s_add_i32 s77, s77, 2
	s_cmp_lt_u32 s77, 16
	s_cbranch_scc1 .Lkl_m1pre_yl

; #define G_WAIT_V(n) asm volatile("s_waitcnt vmcnt(" #n ")" ::: "memory")
; #define G_BAR() __builtin_amdgcn_s_barrier()
; #define G_SCHED() __builtin_amdgcn_sched_barrier(0)
; #define D_STAGE_A(slot, half, kt) D_STAGE(rsA, voffA, slot, half, kt)
; #define D_STAGE_B(slot, half, kt) D_STAGE(rsB, voffB, slot, half, kt)
; #define D_LDA(dst, slot) do { _Pragma("unroll") for (int m = 0; m < 4; ++m) _Pragma("unroll") for (int k = 0; k < 2; ++k) \
;     dst[m][k] = *(const LDS_AS bf16x8*)(lds + (slot) + aoff + m * 2048 + k * 1024); } while (0)
; #define D_LDB(dst, slot) do { _Pragma("unroll") for (int n = 0; n < 2; ++n) _Pragma("unroll") for (int k = 0; k < 2; ++k) \
;     dst[n][k] = *(const LDS_AS bf16x8*)(lds + (slot) + boff + n * 2048 + k * 1024); } while (0)
; #define D_MMA(ai, bj, At, Bf) do { __builtin_amdgcn_s_setprio(1); _Pragma("unroll") for (int m = 0; m < 4; ++m) _Pragma("unroll") for (int n = 0; n < 2; ++n) _Pragma("unroll") for (int k = 0; k < 2; ++k) \
;     acc[ai][bj][m][n] = __builtin_amdgcn_mfma_f32_16x16x32_bf16(Bf[n][k], At[m][k], acc[ai][bj][m][n], 0, 0, 0); __builtin_amdgcn_s_setprio(0); } while (0)
; #define D_WAIT_L(n) asm volatile("s_waitcnt lgkmcnt(" #n ")" ::: "memory")
; #define D_STAGE_A(slot, half, kt) D_STAGE(rsA, voffA, slot, half, kt)
; #define D_STAGE_B(slot, half, kt) do { _Pragma("unroll") for (int _i = 0; _i < 2; ++_i) { const unsigned _m0 = ldsw + (unsigned)((slot) + _i * 8192); const unsigned _so = (unsigned)(kt) * 128u + (half) * bt_half + _i * bt_piece; \
;     asm volatile("s_mov_b32 m0, %0\n\ts_nop 4\n\tbuffer_load_dwordx4 %1, %2, %3 offen lds" :: "s"(_m0), "v"(voffB0), "s"(rsB), "s"(_so) : "m0", "memory"); } } while (0)
; #define D_WAIT_L(n) asm volatile("s_waitcnt lgkmcnt(" #n ")" ::: "memory")
;     ...
;     D_LDB(B0, G_SB(0, 0)); G_SCHED(); D_LDA(At, G_SA(0, 0)); D_STAGE_A(G_SA(1, 1), 1, t1);
;     D_WAIT_L(8); G_BAR(); D_WAIT_L(0); G_SCHED(); D_MMA(0, 0, At, B0); G_BAR(); G_SCHED();
;     D_LDB(B1, G_SB(0, 1)); D_STAGE_B(G_SB(0, 0), 0, t2);
;     G_BAR(); D_WAIT_L(0); G_SCHED(); D_MMA(0, 1, At, B1); G_BAR(); G_SCHED();
;     D_LDA(At, G_SA(0, 1)); D_STAGE_A(G_SA(0, 0), 0, t2);
;     G_BAR(); D_WAIT_L(0); G_SCHED(); D_MMA(1, 0, At, B0); G_BAR(); G_SCHED();
;     D_STAGE_B(G_SB(0, 1), 1, t2);
;     G_WAIT_V(6); G_BAR(); G_SCHED(); D_MMA(1, 1, At, B1); G_BAR(); G_SCHED();
.Lkl_m2npre_yl:
	ds_read_b128 v[198:201], v214
	ds_read_b128 v[202:205], v215
	ds_read_b128 v[206:209], v214 offset:2048
	ds_read_b128 v[210:213], v215 offset:2048
	ds_read_b128 v[228:231], v220
	ds_read_b128 v[232:235], v221
	ds_read_b128 v[236:239], v220 offset:2048
	ds_read_b128 v[240:243], v221 offset:2048
	ds_read_b128 v[68:71], v135 offset:16
	ds_read_b128 v[72:75], v136 offset:16
	ds_read_b128 v[138:141], v135 offset:2064
	ds_read_b128 v[142:145], v136 offset:2064
	ds_read_b128 v[146:149], v135 offset:4112
	ds_read_b128 v[150:153], v136 offset:4112
	ds_read_b128 v[154:157], v135 offset:6160
	ds_read_b128 v[158:161], v136 offset:6160
	ds_read_b128 v[166:169], v135 offset:16400
	ds_read_b128 v[170:173], v136 offset:16400
	ds_read_b128 v[174:177], v135 offset:18448
	ds_read_b128 v[178:181], v136 offset:18448
	ds_read_b128 v[182:185], v135 offset:20496
	ds_read_b128 v[186:189], v136 offset:20496
	ds_read_b128 v[190:193], v135 offset:22544
	ds_read_b128 v[194:197], v136 offset:22544
	s_waitcnt lgkmcnt(0)
	s_cmp_ge_u32 s74, 14
	s_cbranch_scc1 .Lkl_m2npre_y_nd0
	s_lshl_b32 s69, s74, 7
	s_addk_i32 s69, 0x100
	s_add_i32 s70, s69, 0x20000
	s_add_i32 s71, s69, 0x40000
	s_add_i32 s72, s69, 0x60000
	s_mov_b32 m0, s39
	s_nop 0
	buffer_load_dwordx4 v130, s[4:7], s69 offen lds
	s_mov_b32 m0, s51
	s_nop 0
	buffer_load_dwordx4 v128, s[8:11], s69 offen lds
	s_mov_b32 m0, s50
	s_nop 0
	buffer_load_dwordx4 v130, s[4:7], s70 offen lds
	s_mov_b32 m0, s54
	s_nop 0
	buffer_load_dwordx4 v131, s[8:11], s69 offen lds
	s_mov_b32 m0, s55
	s_nop 0
	buffer_load_dwordx4 v130, s[4:7], s71 offen lds
	s_mov_b32 m0, s59
	s_nop 0
	buffer_load_dwordx4 v129, s[8:11], s69 offen lds
	s_mov_b32 m0, s58
	s_nop 0
	buffer_load_dwordx4 v130, s[4:7], s72 offen lds
	s_mov_b32 m0, s60
	s_nop 0
	buffer_load_dwordx4 v132, s[8:11], s69 offen lds
	s_waitcnt vmcnt(8)
	s_branch .Lkl_m2npre_y_nd0_j

; #define G_WAIT_V(n) asm volatile("s_waitcnt vmcnt(" #n ")" ::: "memory")
; #define G_BAR() __builtin_amdgcn_s_barrier()
; #define G_SCHED() __builtin_amdgcn_sched_barrier(0)
; #define D_STAGE_A(slot, half, kt) D_STAGE(rsA, voffA, slot, half, kt)
; #define D_STAGE_B(slot, half, kt) D_STAGE(rsB, voffB, slot, half, kt)
; #define D_LDA(dst, slot) do { _Pragma("unroll") for (int m = 0; m < 4; ++m) _Pragma("unroll") for (int k = 0; k < 2; ++k) \
;     dst[m][k] = *(const LDS_AS bf16x8*)(lds + (slot) + aoff + m * 2048 + k * 1024); } while (0)
; #define D_LDB(dst, slot) do { _Pragma("unroll") for (int n = 0; n < 2; ++n) _Pragma("unroll") for (int k = 0; k < 2; ++k) \
;     dst[n][k] = *(const LDS_AS bf16x8*)(lds + (slot) + boff + n * 2048 + k * 1024); } while (0)
; #define D_MMA(ai, bj, At, Bf) do { __builtin_amdgcn_s_setprio(1); _Pragma("unroll") for (int m = 0; m < 4; ++m) _Pragma("unroll") for (int n = 0; n < 2; ++n) _Pragma("unroll") for (int k = 0; k < 2; ++k) \
;     acc[ai][bj][m][n] = __builtin_amdgcn_mfma_f32_16x16x32_bf16(Bf[n][k], At[m][k], acc[ai][bj][m][n], 0, 0, 0); __builtin_amdgcn_s_setprio(0); } while (0)
; #define D_WAIT_L(n) asm volatile("s_waitcnt lgkmcnt(" #n ")" ::: "memory")
;     ...
;     D_LDB(B0, G_SB(0, 0)); G_SCHED(); D_LDA(At, G_SA(0, 0)); D_STAGE_A(G_SA(1, 1), 1, t1);
;     D_WAIT_L(8); G_BAR(); D_WAIT_L(0); G_SCHED(); D_MMA(0, 0, At, B0); G_BAR(); G_SCHED();
;     D_LDB(B1, G_SB(0, 1)); D_STAGE_B(G_SB(0, 0), 0, t2);
;     G_BAR(); D_WAIT_L(0); G_SCHED(); D_MMA(0, 1, At, B1); G_BAR(); G_SCHED();
;     D_LDA(At, G_SA(0, 1)); D_STAGE_A(G_SA(0, 0), 0, t2);
;     G_BAR(); D_WAIT_L(0); G_SCHED(); D_MMA(1, 0, At, B0); G_BAR(); G_SCHED();
;     D_STAGE_B(G_SB(0, 1), 1, t2);
;     G_WAIT_V(6); G_BAR(); G_SCHED(); D_MMA(1, 1, At, B1); G_BAR(); G_SCHED();
;     D_LDB(B0, G_SB(1, 0)); G_SCHED(); D_LDA(At, G_SA(1, 0)); D_STAGE_A(G_SA(0, 1), 1, t2);
;     D_WAIT_L(8); G_BAR(); D_WAIT_L(0); G_SCHED(); D_MMA(0, 0, At, B0); G_BAR(); G_SCHED();
;     D_LDB(B1, G_SB(1, 1)); D_STAGE_B(G_SB(1, 0), 0, t3);
;     G_BAR(); D_WAIT_L(0); G_SCHED(); D_MMA(0, 1, At, B1); G_BAR(); G_SCHED();
;     D_LDA(At, G_SA(1, 1)); D_STAGE_A(G_SA(1, 0), 0, t3);
;     G_BAR(); D_WAIT_L(0); G_SCHED(); D_MMA(1, 0, At, B0); G_BAR(); G_SCHED();
;     D_STAGE_B(G_SB(1, 1), 1, t3);
;     G_WAIT_V(6); G_BAR(); G_SCHED(); D_MMA(1, 1, At, B1); G_BAR(); G_SCHED();
.Lkl_m2npre_y_nd0_j:
	s_barrier
	s_setprio 1
	v_mfma_scale_f32_16x16x128_f8f6f4 v[124:127], v[198:205], v[68:75], v[124:127], v165, v164 op_sel_hi:[0,0,0]
	v_mfma_scale_f32_16x16x128_f8f6f4 v[120:123], v[206:213], v[68:75], v[120:123], v165, v164 op_sel_hi:[0,0,0]
	v_mfma_scale_f32_16x16x128_f8f6f4 v[108:111], v[198:205], v[138:145], v[108:111], v165, v164 op_sel_hi:[0,0,0]
	v_mfma_scale_f32_16x16x128_f8f6f4 v[100:103], v[206:213], v[138:145], v[100:103], v165, v164 op_sel_hi:[0,0,0]
	v_mfma_scale_f32_16x16x128_f8f6f4 v[84:87], v[198:205], v[146:153], v[84:87], v165, v164 op_sel_hi:[0,0,0]
	v_mfma_scale_f32_16x16x128_f8f6f4 v[80:83], v[206:213], v[146:153], v[80:83], v165, v164 op_sel_hi:[0,0,0]
	v_mfma_scale_f32_16x16x128_f8f6f4 v[216:219], v[198:205], v[154:161], v[216:219], v165, v164 op_sel_hi:[0,0,0]
	v_mfma_scale_f32_16x16x128_f8f6f4 v[48:51], v[206:213], v[154:161], v[48:51], v165, v164 op_sel_hi:[0,0,0]
	v_mfma_scale_f32_16x16x128_f8f6f4 v[116:119], v[228:235], v[68:75], v[116:119], v165, v164 op_sel_hi:[0,0,0]
	v_mfma_scale_f32_16x16x128_f8f6f4 v[112:115], v[236:243], v[68:75], v[112:115], v165, v164 op_sel_hi:[0,0,0]
	v_mfma_scale_f32_16x16x128_f8f6f4 v[104:107], v[228:235], v[138:145], v[104:107], v165, v164 op_sel_hi:[0,0,0]
	v_mfma_scale_f32_16x16x128_f8f6f4 v[96:99], v[236:243], v[138:145], v[96:99], v165, v164 op_sel_hi:[0,0,0]
	v_mfma_scale_f32_16x16x128_f8f6f4 v[92:95], v[228:235], v[146:153], v[92:95], v165, v164 op_sel_hi:[0,0,0]
	v_mfma_scale_f32_16x16x128_f8f6f4 v[88:91], v[236:243], v[146:153], v[88:91], v165, v164 op_sel_hi:[0,0,0]
	v_mfma_scale_f32_16x16x128_f8f6f4 v[76:79], v[228:235], v[154:161], v[76:79], v165, v164 op_sel_hi:[0,0,0]
	v_mfma_scale_f32_16x16x128_f8f6f4 v[16:19], v[236:243], v[154:161], v[16:19], v165, v164 op_sel_hi:[0,0,0]
	v_mfma_scale_f32_16x16x128_f8f6f4 v[56:59], v[198:205], v[166:173], v[56:59], v165, v164 op_sel_hi:[0,0,0]
	v_mfma_scale_f32_16x16x128_f8f6f4 v[52:55], v[206:213], v[166:173], v[52:55], v165, v164 op_sel_hi:[0,0,0]
	v_mfma_scale_f32_16x16x128_f8f6f4 v[36:39], v[198:205], v[174:181], v[36:39], v165, v164 op_sel_hi:[0,0,0]
	v_mfma_scale_f32_16x16x128_f8f6f4 v[32:35], v[206:213], v[174:181], v[32:35], v165, v164 op_sel_hi:[0,0,0]
	v_mfma_scale_f32_16x16x128_f8f6f4 v[20:23], v[198:205], v[182:189], v[20:23], v165, v164 op_sel_hi:[0,0,0]
	v_mfma_scale_f32_16x16x128_f8f6f4 v[224:227], v[206:213], v[182:189], v[224:227], v165, v164 op_sel_hi:[0,0,0]
	v_mfma_scale_f32_16x16x128_f8f6f4 v[4:7], v[198:205], v[190:197], v[4:7], v165, v164 op_sel_hi:[0,0,0]
	v_mfma_scale_f32_16x16x128_f8f6f4 v[0:3], v[206:213], v[190:197], v[0:3], v165, v164 op_sel_hi:[0,0,0]
	v_mfma_scale_f32_16x16x128_f8f6f4 v[64:67], v[228:235], v[166:173], v[64:67], v165, v164 op_sel_hi:[0,0,0]
	v_mfma_scale_f32_16x16x128_f8f6f4 v[60:63], v[236:243], v[166:173], v[60:63], v165, v164 op_sel_hi:[0,0,0]
	v_mfma_scale_f32_16x16x128_f8f6f4 v[44:47], v[228:235], v[174:181], v[44:47], v165, v164 op_sel_hi:[0,0,0]
	v_mfma_scale_f32_16x16x128_f8f6f4 v[40:43], v[236:243], v[174:181], v[40:43], v165, v164 op_sel_hi:[0,0,0]
	v_mfma_scale_f32_16x16x128_f8f6f4 v[28:31], v[228:235], v[182:189], v[28:31], v165, v164 op_sel_hi:[0,0,0]
	v_mfma_scale_f32_16x16x128_f8f6f4 v[24:27], v[236:243], v[182:189], v[24:27], v165, v164 op_sel_hi:[0,0,0]
	v_mfma_scale_f32_16x16x128_f8f6f4 v[12:15], v[228:235], v[190:197], v[12:15], v165, v164 op_sel_hi:[0,0,0]
	v_mfma_scale_f32_16x16x128_f8f6f4 v[8:11], v[236:243], v[190:197], v[8:11], v165, v164 op_sel_hi:[0,0,0]
	s_setprio 0
	s_barrier
	ds_read_b128 v[198:201], v222
	ds_read_b128 v[202:205], v223
	ds_read_b128 v[206:209], v222 offset:2048
	ds_read_b128 v[210:213], v223 offset:2048
	ds_read_b128 v[228:231], v244
	ds_read_b128 v[232:235], v245
	ds_read_b128 v[236:239], v244 offset:2048
	ds_read_b128 v[240:243], v245 offset:2048
	ds_read_b128 v[68:71], v135 offset:32784
	ds_read_b128 v[72:75], v136 offset:32784
	ds_read_b128 v[138:141], v135 offset:34832
	ds_read_b128 v[142:145], v136 offset:34832
	ds_read_b128 v[146:149], v135 offset:36880
	ds_read_b128 v[150:153], v136 offset:36880
	ds_read_b128 v[154:157], v135 offset:38928
	ds_read_b128 v[158:161], v136 offset:38928
	ds_read_b128 v[166:169], v135 offset:49168
	ds_read_b128 v[170:173], v136 offset:49168
	ds_read_b128 v[174:177], v135 offset:51216
	ds_read_b128 v[178:181], v136 offset:51216
	ds_read_b128 v[182:185], v135 offset:53264
	ds_read_b128 v[186:189], v136 offset:53264
	ds_read_b128 v[190:193], v135 offset:55312
	ds_read_b128 v[194:197], v136 offset:55312
	s_waitcnt lgkmcnt(0)
	s_cmp_ge_u32 s74, 14
	s_cbranch_scc1 .Lkl_m2npre_y_nd1
	s_lshl_b32 s69, s74, 7
	s_addk_i32 s69, 0x180
	s_add_i32 s70, s69, 0x20000
	s_add_i32 s71, s69, 0x40000
	s_add_i32 s72, s69, 0x60000
	s_mov_b32 m0, s61
	s_nop 0
	buffer_load_dwordx4 v130, s[4:7], s69 offen lds
	s_mov_b32 m0, s63
	s_nop 0
	buffer_load_dwordx4 v128, s[8:11], s69 offen lds
	s_mov_b32 m0, s62
	s_nop 0
	buffer_load_dwordx4 v130, s[4:7], s70 offen lds
	s_mov_b32 m0, s64
	s_nop 0
	buffer_load_dwordx4 v131, s[8:11], s69 offen lds
	s_mov_b32 m0, s65
	s_nop 0
	buffer_load_dwordx4 v130, s[4:7], s71 offen lds
	s_mov_b32 m0, s67
	s_nop 0
	buffer_load_dwordx4 v129, s[8:11], s69 offen lds
	s_mov_b32 m0, s66
	s_nop 0
	buffer_load_dwordx4 v130, s[4:7], s72 offen lds
	s_mov_b32 m0, s68
	s_nop 0
	buffer_load_dwordx4 v132, s[8:11], s69 offen lds
	s_waitcnt vmcnt(8)
	s_branch .Lkl_m2npre_y_nd1_j

; #define G_WAIT_V(n) asm volatile("s_waitcnt vmcnt(" #n ")" ::: "memory")
; #define G_BAR() __builtin_amdgcn_s_barrier()
; #define G_SCHED() __builtin_amdgcn_sched_barrier(0)
; #define D_STAGE_A(slot, half, kt) D_STAGE(rsA, voffA, slot, half, kt)
; #define D_STAGE_B(slot, half, kt) D_STAGE(rsB, voffB, slot, half, kt)
; #define D_LDA(dst, slot) do { _Pragma("unroll") for (int m = 0; m < 4; ++m) _Pragma("unroll") for (int k = 0; k < 2; ++k) \
;     dst[m][k] = *(const LDS_AS bf16x8*)(lds + (slot) + aoff + m * 2048 + k * 1024); } while (0)
; #define D_LDB(dst, slot) do { _Pragma("unroll") for (int n = 0; n < 2; ++n) _Pragma("unroll") for (int k = 0; k < 2; ++k) \
;     dst[n][k] = *(const LDS_AS bf16x8*)(lds + (slot) + boff + n * 2048 + k * 1024); } while (0)
; #define D_MMA(ai, bj, At, Bf) do { __builtin_amdgcn_s_setprio(1); _Pragma("unroll") for (int m = 0; m < 4; ++m) _Pragma("unroll") for (int n = 0; n < 2; ++n) _Pragma("unroll") for (int k = 0; k < 2; ++k) \
;     acc[ai][bj][m][n] = __builtin_amdgcn_mfma_f32_16x16x32_bf16(Bf[n][k], At[m][k], acc[ai][bj][m][n], 0, 0, 0); __builtin_amdgcn_s_setprio(0); } while (0)
; #define D_WAIT_L(n) asm volatile("s_waitcnt lgkmcnt(" #n ")" ::: "memory")
; #define D_STAGE_A(slot, half, kt) D_STAGE(rsA, voffA, slot, half, kt)
; #define D_STAGE_B(slot, half, kt) do { _Pragma("unroll") for (int _i = 0; _i < 2; ++_i) { const unsigned _m0 = ldsw + (unsigned)((slot) + _i * 8192); const unsigned _so = (unsigned)(kt) * 128u + (half) * bt_half + _i * bt_piece; \
;     asm volatile("s_mov_b32 m0, %0\n\ts_nop 4\n\tbuffer_load_dwordx4 %1, %2, %3 offen lds" :: "s"(_m0), "v"(voffB0), "s"(rsB), "s"(_so) : "m0", "memory"); } } while (0)
; #define D_WAIT_L(n) asm volatile("s_waitcnt lgkmcnt(" #n ")" ::: "memory")
;     ...
;     D_LDB(B0, G_SB(1, 0)); G_SCHED(); D_LDA(At, G_SA(1, 0)); D_STAGE_A(G_SA(0, 1), 1, t2);
;     D_WAIT_L(8); G_BAR(); D_WAIT_L(0); G_SCHED(); D_MMA(0, 0, At, B0); G_BAR(); G_SCHED();
;     D_LDB(B1, G_SB(1, 1)); D_STAGE_B(G_SB(1, 0), 0, t3);
;     G_BAR(); D_WAIT_L(0); G_SCHED(); D_MMA(0, 1, At, B1); G_BAR(); G_SCHED();
;     D_LDA(At, G_SA(1, 1)); D_STAGE_A(G_SA(1, 0), 0, t3);
;     G_BAR(); D_WAIT_L(0); G_SCHED(); D_MMA(1, 0, At, B0); G_BAR(); G_SCHED();
;     D_STAGE_B(G_SB(1, 1), 1, t3);
;     G_WAIT_V(6); G_BAR(); G_SCHED(); D_MMA(1, 1, At, B1); G_BAR(); G_SCHED();
;   }
.Lkl_m2npre_y_nd1_j:
	s_barrier
	s_setprio 1
	v_mfma_scale_f32_16x16x128_f8f6f4 v[124:127], v[198:205], v[68:75], v[124:127], v165, v164 op_sel_hi:[0,0,0]
	v_mfma_scale_f32_16x16x128_f8f6f4 v[120:123], v[206:213], v[68:75], v[120:123], v165, v164 op_sel_hi:[0,0,0]
	v_mfma_scale_f32_16x16x128_f8f6f4 v[108:111], v[198:205], v[138:145], v[108:111], v165, v164 op_sel_hi:[0,0,0]
	v_mfma_scale_f32_16x16x128_f8f6f4 v[100:103], v[206:213], v[138:145], v[100:103], v165, v164 op_sel_hi:[0,0,0]
	v_mfma_scale_f32_16x16x128_f8f6f4 v[84:87], v[198:205], v[146:153], v[84:87], v165, v164 op_sel_hi:[0,0,0]
	v_mfma_scale_f32_16x16x128_f8f6f4 v[80:83], v[206:213], v[146:153], v[80:83], v165, v164 op_sel_hi:[0,0,0]
	v_mfma_scale_f32_16x16x128_f8f6f4 v[216:219], v[198:205], v[154:161], v[216:219], v165, v164 op_sel_hi:[0,0,0]
	v_mfma_scale_f32_16x16x128_f8f6f4 v[48:51], v[206:213], v[154:161], v[48:51], v165, v164 op_sel_hi:[0,0,0]
	v_mfma_scale_f32_16x16x128_f8f6f4 v[116:119], v[228:235], v[68:75], v[116:119], v165, v164 op_sel_hi:[0,0,0]
	v_mfma_scale_f32_16x16x128_f8f6f4 v[112:115], v[236:243], v[68:75], v[112:115], v165, v164 op_sel_hi:[0,0,0]
	v_mfma_scale_f32_16x16x128_f8f6f4 v[104:107], v[228:235], v[138:145], v[104:107], v165, v164 op_sel_hi:[0,0,0]
	v_mfma_scale_f32_16x16x128_f8f6f4 v[96:99], v[236:243], v[138:145], v[96:99], v165, v164 op_sel_hi:[0,0,0]
	v_mfma_scale_f32_16x16x128_f8f6f4 v[92:95], v[228:235], v[146:153], v[92:95], v165, v164 op_sel_hi:[0,0,0]
	v_mfma_scale_f32_16x16x128_f8f6f4 v[88:91], v[236:243], v[146:153], v[88:91], v165, v164 op_sel_hi:[0,0,0]
	v_mfma_scale_f32_16x16x128_f8f6f4 v[76:79], v[228:235], v[154:161], v[76:79], v165, v164 op_sel_hi:[0,0,0]
	v_mfma_scale_f32_16x16x128_f8f6f4 v[16:19], v[236:243], v[154:161], v[16:19], v165, v164 op_sel_hi:[0,0,0]
	v_mfma_scale_f32_16x16x128_f8f6f4 v[56:59], v[198:205], v[166:173], v[56:59], v165, v164 op_sel_hi:[0,0,0]
	v_mfma_scale_f32_16x16x128_f8f6f4 v[52:55], v[206:213], v[166:173], v[52:55], v165, v164 op_sel_hi:[0,0,0]
	v_mfma_scale_f32_16x16x128_f8f6f4 v[36:39], v[198:205], v[174:181], v[36:39], v165, v164 op_sel_hi:[0,0,0]
	v_mfma_scale_f32_16x16x128_f8f6f4 v[32:35], v[206:213], v[174:181], v[32:35], v165, v164 op_sel_hi:[0,0,0]
	v_mfma_scale_f32_16x16x128_f8f6f4 v[20:23], v[198:205], v[182:189], v[20:23], v165, v164 op_sel_hi:[0,0,0]
	v_mfma_scale_f32_16x16x128_f8f6f4 v[224:227], v[206:213], v[182:189], v[224:227], v165, v164 op_sel_hi:[0,0,0]
	v_mfma_scale_f32_16x16x128_f8f6f4 v[4:7], v[198:205], v[190:197], v[4:7], v165, v164 op_sel_hi:[0,0,0]
	v_mfma_scale_f32_16x16x128_f8f6f4 v[0:3], v[206:213], v[190:197], v[0:3], v165, v164 op_sel_hi:[0,0,0]
	v_mfma_scale_f32_16x16x128_f8f6f4 v[64:67], v[228:235], v[166:173], v[64:67], v165, v164 op_sel_hi:[0,0,0]
	v_mfma_scale_f32_16x16x128_f8f6f4 v[60:63], v[236:243], v[166:173], v[60:63], v165, v164 op_sel_hi:[0,0,0]
	v_mfma_scale_f32_16x16x128_f8f6f4 v[44:47], v[228:235], v[174:181], v[44:47], v165, v164 op_sel_hi:[0,0,0]
	v_mfma_scale_f32_16x16x128_f8f6f4 v[40:43], v[236:243], v[174:181], v[40:43], v165, v164 op_sel_hi:[0,0,0]
	v_mfma_scale_f32_16x16x128_f8f6f4 v[28:31], v[228:235], v[182:189], v[28:31], v165, v164 op_sel_hi:[0,0,0]
	v_mfma_scale_f32_16x16x128_f8f6f4 v[24:27], v[236:243], v[182:189], v[24:27], v165, v164 op_sel_hi:[0,0,0]
	v_mfma_scale_f32_16x16x128_f8f6f4 v[12:15], v[228:235], v[190:197], v[12:15], v165, v164 op_sel_hi:[0,0,0]
	v_mfma_scale_f32_16x16x128_f8f6f4 v[8:11], v[236:243], v[190:197], v[8:11], v165, v164 op_sel_hi:[0,0,0]
	s_setprio 0
	s_barrier
	s_add_i32 s74, s74, 2
	s_cmp_lt_u32 s74, 16
	s_cbranch_scc1 .Lkl_m2npre_yl

; #define G_WAIT_V(n) asm volatile("s_waitcnt vmcnt(" #n ")" ::: "memory")
; #define G_BAR() __builtin_amdgcn_s_barrier()
; #define G_SCHED() __builtin_amdgcn_sched_barrier(0)
; #define D_STAGE_A(slot, half, kt) D_STAGE(rsA, voffA, slot, half, kt)
; #define D_STAGE_B(slot, half, kt) D_STAGE(rsB, voffB, slot, half, kt)
; #define D_LDA(dst, slot) do { _Pragma("unroll") for (int m = 0; m < 4; ++m) _Pragma("unroll") for (int k = 0; k < 2; ++k) \
;     dst[m][k] = *(const LDS_AS bf16x8*)(lds + (slot) + aoff + m * 2048 + k * 1024); } while (0)
; #define D_LDB(dst, slot) do { _Pragma("unroll") for (int n = 0; n < 2; ++n) _Pragma("unroll") for (int k = 0; k < 2; ++k) \
;     dst[n][k] = *(const LDS_AS bf16x8*)(lds + (slot) + boff + n * 2048 + k * 1024); } while (0)
; #define D_MMA(ai, bj, At, Bf) do { __builtin_amdgcn_s_setprio(1); _Pragma("unroll") for (int m = 0; m < 4; ++m) _Pragma("unroll") for (int n = 0; n < 2; ++n) _Pragma("unroll") for (int k = 0; k < 2; ++k) \
;     acc[ai][bj][m][n] = __builtin_amdgcn_mfma_f32_16x16x32_bf16(Bf[n][k], At[m][k], acc[ai][bj][m][n], 0, 0, 0); __builtin_amdgcn_s_setprio(0); } while (0)
; #define D_WAIT_L(n) asm volatile("s_waitcnt lgkmcnt(" #n ")" ::: "memory")
; #define D_STAGE_A(slot, half, kt) D_STAGE(rsA, voffA, slot, half, kt)
; #define D_STAGE_B(slot, half, kt) do { _Pragma("unroll") for (int _i = 0; _i < 2; ++_i) { const unsigned _m0 = ldsw + (unsigned)((slot) + _i * 8192); const unsigned _so = (unsigned)(kt) * 128u + (half) * bt_half + _i * bt_piece; \
;     asm volatile("s_mov_b32 m0, %0\n\ts_nop 4\n\tbuffer_load_dwordx4 %1, %2, %3 offen lds" :: "s"(_m0), "v"(voffB0), "s"(rsB), "s"(_so) : "m0", "memory"); } } while (0)
; #define D_WAIT_L(n) asm volatile("s_waitcnt lgkmcnt(" #n ")" ::: "memory")
;     ...
;     D_LDB(B0, G_SB(0, 0)); G_SCHED(); D_LDA(At, G_SA(0, 0)); D_STAGE_A(G_SA(1, 1), 1, t1);
;     D_WAIT_L(8); G_BAR(); D_WAIT_L(0); G_SCHED(); D_MMA(0, 0, At, B0); G_BAR(); G_SCHED();
;     D_LDB(B1, G_SB(0, 1)); D_STAGE_B(G_SB(0, 0), 0, t2);
;     G_BAR(); D_WAIT_L(0); G_SCHED(); D_MMA(0, 1, At, B1); G_BAR(); G_SCHED();
;     D_LDA(At, G_SA(0, 1)); D_STAGE_A(G_SA(0, 0), 0, t2);
;     G_BAR(); D_WAIT_L(0); G_SCHED(); D_MMA(1, 0, At, B0); G_BAR(); G_SCHED();
;     D_STAGE_B(G_SB(0, 1), 1, t2);
;     G_WAIT_V(6); G_BAR(); G_SCHED(); D_MMA(1, 1, At, B1); G_BAR(); G_SCHED();
.Lkl_m2pre_yl:
	ds_read_b128 v[208:211], v68
	ds_read_b128 v[212:215], v69
	ds_read_b128 v[224:227], v68 offset:2048
	ds_read_b128 v[228:231], v69 offset:2048
	ds_read_b128 v[232:235], v70
	ds_read_b128 v[236:239], v71
	ds_read_b128 v[240:243], v70 offset:2048
	ds_read_b128 v[244:247], v71 offset:2048
	ds_read_b128 v[138:141], v135 offset:16
	ds_read_b128 v[142:145], v136 offset:16
	ds_read_b128 v[146:149], v135 offset:2064
	ds_read_b128 v[150:153], v136 offset:2064
	ds_read_b128 v[154:157], v135 offset:4112
	ds_read_b128 v[158:161], v136 offset:4112
	ds_read_b128 v[168:171], v135 offset:6160
	ds_read_b128 v[172:175], v136 offset:6160
	ds_read_b128 v[176:179], v135 offset:16400
	ds_read_b128 v[180:183], v136 offset:16400
	ds_read_b128 v[184:187], v135 offset:18448
	ds_read_b128 v[188:191], v136 offset:18448
	ds_read_b128 v[192:195], v135 offset:20496
	ds_read_b128 v[196:199], v136 offset:20496
	ds_read_b128 v[200:203], v135 offset:22544
	ds_read_b128 v[204:207], v136 offset:22544
	s_waitcnt lgkmcnt(0)
	s_cmp_ge_u32 s68, 14
	s_cbranch_scc1 .Lkl_m2pre_y_nd0
	s_lshl_b32 s63, s68, 7
	s_addk_i32 s63, 0x100
	s_add_i32 s64, s63, 0x20000
	s_add_i32 s65, s63, 0x40000
	s_add_i32 s66, s63, 0x60000
	s_mov_b32 m0, s25
	s_nop 0
	buffer_load_dwordx4 v134, s[4:7], s63 offen lds
	s_mov_b32 m0, s15
	s_nop 0
	buffer_load_dwordx4 v162, s[8:11], s63 offen lds
	s_mov_b32 m0, s54
	s_nop 0
	buffer_load_dwordx4 v134, s[4:7], s64 offen lds
	s_mov_b32 m0, s55
	s_nop 0
	buffer_load_dwordx4 v163, s[8:11], s63 offen lds
	s_mov_b32 m0, s26
	s_nop 0
	buffer_load_dwordx4 v134, s[4:7], s65 offen lds
	s_mov_b32 m0, s27
	s_nop 0
	buffer_load_dwordx4 v166, s[8:11], s63 offen lds
	s_mov_b32 m0, s58
	s_nop 0
	buffer_load_dwordx4 v134, s[4:7], s66 offen lds
	s_mov_b32 m0, s59
	s_nop 0
	buffer_load_dwordx4 v167, s[8:11], s63 offen lds
	s_waitcnt vmcnt(8)
	s_branch .Lkl_m2pre_y_nd0_j

; #define G_WAIT_V(n) asm volatile("s_waitcnt vmcnt(" #n ")" ::: "memory")
; #define G_BAR() __builtin_amdgcn_s_barrier()
; #define G_SCHED() __builtin_amdgcn_sched_barrier(0)
; #define D_STAGE_A(slot, half, kt) D_STAGE(rsA, voffA, slot, half, kt)
; #define D_STAGE_B(slot, half, kt) D_STAGE(rsB, voffB, slot, half, kt)
; #define D_LDA(dst, slot) do { _Pragma("unroll") for (int m = 0; m < 4; ++m) _Pragma("unroll") for (int k = 0; k < 2; ++k) \
;     dst[m][k] = *(const LDS_AS bf16x8*)(lds + (slot) + aoff + m * 2048 + k * 1024); } while (0)
; #define D_LDB(dst, slot) do { _Pragma("unroll") for (int n = 0; n < 2; ++n) _Pragma("unroll") for (int k = 0; k < 2; ++k) \
;     dst[n][k] = *(const LDS_AS bf16x8*)(lds + (slot) + boff + n * 2048 + k * 1024); } while (0)
; #define D_MMA(ai, bj, At, Bf) do { __builtin_amdgcn_s_setprio(1); _Pragma("unroll") for (int m = 0; m < 4; ++m) _Pragma("unroll") for (int n = 0; n < 2; ++n) _Pragma("unroll") for (int k = 0; k < 2; ++k) \
;     acc[ai][bj][m][n] = __builtin_amdgcn_mfma_f32_16x16x32_bf16(Bf[n][k], At[m][k], acc[ai][bj][m][n], 0, 0, 0); __builtin_amdgcn_s_setprio(0); } while (0)
; #define D_WAIT_L(n) asm volatile("s_waitcnt lgkmcnt(" #n ")" ::: "memory")
;     ...
;     D_LDB(B0, G_SB(0, 0)); G_SCHED(); D_LDA(At, G_SA(0, 0)); D_STAGE_A(G_SA(1, 1), 1, t1);
;     D_WAIT_L(8); G_BAR(); D_WAIT_L(0); G_SCHED(); D_MMA(0, 0, At, B0); G_BAR(); G_SCHED();
;     D_LDB(B1, G_SB(0, 1)); D_STAGE_B(G_SB(0, 0), 0, t2);
;     G_BAR(); D_WAIT_L(0); G_SCHED(); D_MMA(0, 1, At, B1); G_BAR(); G_SCHED();
;     D_LDA(At, G_SA(0, 1)); D_STAGE_A(G_SA(0, 0), 0, t2);
;     G_BAR(); D_WAIT_L(0); G_SCHED(); D_MMA(1, 0, At, B0); G_BAR(); G_SCHED();
;     D_STAGE_B(G_SB(0, 1), 1, t2);
;     G_WAIT_V(6); G_BAR(); G_SCHED(); D_MMA(1, 1, At, B1); G_BAR(); G_SCHED();
;     D_LDB(B0, G_SB(1, 0)); G_SCHED(); D_LDA(At, G_SA(1, 0)); D_STAGE_A(G_SA(0, 1), 1, t2);
;     D_WAIT_L(8); G_BAR(); D_WAIT_L(0); G_SCHED(); D_MMA(0, 0, At, B0); G_BAR(); G_SCHED();
;     D_LDB(B1, G_SB(1, 1)); D_STAGE_B(G_SB(1, 0), 0, t3);
;     G_BAR(); D_WAIT_L(0); G_SCHED(); D_MMA(0, 1, At, B1); G_BAR(); G_SCHED();
;     D_LDA(At, G_SA(1, 1)); D_STAGE_A(G_SA(1, 0), 0, t3);
;     G_BAR(); D_WAIT_L(0); G_SCHED(); D_MMA(1, 0, At, B0); G_BAR(); G_SCHED();
;     D_STAGE_B(G_SB(1, 1), 1, t3);
;     G_WAIT_V(6); G_BAR(); G_SCHED(); D_MMA(1, 1, At, B1); G_BAR(); G_SCHED();
.Lkl_m2pre_y_nd0_j:
	s_barrier
	s_setprio 1
	v_mfma_scale_f32_16x16x128_f8f6f4 v[124:127], v[208:215], v[138:145], v[124:127], v165, v164 op_sel_hi:[0,0,0]
	v_mfma_scale_f32_16x16x128_f8f6f4 v[120:123], v[224:231], v[138:145], v[120:123], v165, v164 op_sel_hi:[0,0,0]
	v_mfma_scale_f32_16x16x128_f8f6f4 v[108:111], v[208:215], v[146:153], v[108:111], v165, v164 op_sel_hi:[0,0,0]
	v_mfma_scale_f32_16x16x128_f8f6f4 v[100:103], v[224:231], v[146:153], v[100:103], v165, v164 op_sel_hi:[0,0,0]
	v_mfma_scale_f32_16x16x128_f8f6f4 v[84:87], v[208:215], v[154:161], v[84:87], v165, v164 op_sel_hi:[0,0,0]
	v_mfma_scale_f32_16x16x128_f8f6f4 v[80:83], v[224:231], v[154:161], v[80:83], v165, v164 op_sel_hi:[0,0,0]
	v_mfma_scale_f32_16x16x128_f8f6f4 v[220:223], v[208:215], v[168:175], v[220:223], v165, v164 op_sel_hi:[0,0,0]
	v_mfma_scale_f32_16x16x128_f8f6f4 v[48:51], v[224:231], v[168:175], v[48:51], v165, v164 op_sel_hi:[0,0,0]
	v_mfma_scale_f32_16x16x128_f8f6f4 v[116:119], v[232:239], v[138:145], v[116:119], v165, v164 op_sel_hi:[0,0,0]
	v_mfma_scale_f32_16x16x128_f8f6f4 v[112:115], v[240:247], v[138:145], v[112:115], v165, v164 op_sel_hi:[0,0,0]
	v_mfma_scale_f32_16x16x128_f8f6f4 v[104:107], v[232:239], v[146:153], v[104:107], v165, v164 op_sel_hi:[0,0,0]
	v_mfma_scale_f32_16x16x128_f8f6f4 v[96:99], v[240:247], v[146:153], v[96:99], v165, v164 op_sel_hi:[0,0,0]
	v_mfma_scale_f32_16x16x128_f8f6f4 v[92:95], v[232:239], v[154:161], v[92:95], v165, v164 op_sel_hi:[0,0,0]
	v_mfma_scale_f32_16x16x128_f8f6f4 v[88:91], v[240:247], v[154:161], v[88:91], v165, v164 op_sel_hi:[0,0,0]
	v_mfma_scale_f32_16x16x128_f8f6f4 v[76:79], v[232:239], v[168:175], v[76:79], v165, v164 op_sel_hi:[0,0,0]
	v_mfma_scale_f32_16x16x128_f8f6f4 v[72:75], v[240:247], v[168:175], v[72:75], v165, v164 op_sel_hi:[0,0,0]
	v_mfma_scale_f32_16x16x128_f8f6f4 v[56:59], v[208:215], v[176:183], v[56:59], v165, v164 op_sel_hi:[0,0,0]
	v_mfma_scale_f32_16x16x128_f8f6f4 v[52:55], v[224:231], v[176:183], v[52:55], v165, v164 op_sel_hi:[0,0,0]
	v_mfma_scale_f32_16x16x128_f8f6f4 v[36:39], v[208:215], v[184:191], v[36:39], v165, v164 op_sel_hi:[0,0,0]
	v_mfma_scale_f32_16x16x128_f8f6f4 v[32:35], v[224:231], v[184:191], v[32:35], v165, v164 op_sel_hi:[0,0,0]
	v_mfma_scale_f32_16x16x128_f8f6f4 v[20:23], v[208:215], v[192:199], v[20:23], v165, v164 op_sel_hi:[0,0,0]
	v_mfma_scale_f32_16x16x128_f8f6f4 v[16:19], v[224:231], v[192:199], v[16:19], v165, v164 op_sel_hi:[0,0,0]
	v_mfma_scale_f32_16x16x128_f8f6f4 v[4:7], v[208:215], v[200:207], v[4:7], v165, v164 op_sel_hi:[0,0,0]
	v_mfma_scale_f32_16x16x128_f8f6f4 v[0:3], v[224:231], v[200:207], v[0:3], v165, v164 op_sel_hi:[0,0,0]
	v_mfma_scale_f32_16x16x128_f8f6f4 v[64:67], v[232:239], v[176:183], v[64:67], v165, v164 op_sel_hi:[0,0,0]
	v_mfma_scale_f32_16x16x128_f8f6f4 v[60:63], v[240:247], v[176:183], v[60:63], v165, v164 op_sel_hi:[0,0,0]
	v_mfma_scale_f32_16x16x128_f8f6f4 v[44:47], v[232:239], v[184:191], v[44:47], v165, v164 op_sel_hi:[0,0,0]
	v_mfma_scale_f32_16x16x128_f8f6f4 v[40:43], v[240:247], v[184:191], v[40:43], v165, v164 op_sel_hi:[0,0,0]
	v_mfma_scale_f32_16x16x128_f8f6f4 v[28:31], v[232:239], v[192:199], v[28:31], v165, v164 op_sel_hi:[0,0,0]
	v_mfma_scale_f32_16x16x128_f8f6f4 v[24:27], v[240:247], v[192:199], v[24:27], v165, v164 op_sel_hi:[0,0,0]
	v_mfma_scale_f32_16x16x128_f8f6f4 v[12:15], v[232:239], v[200:207], v[12:15], v165, v164 op_sel_hi:[0,0,0]
	v_mfma_scale_f32_16x16x128_f8f6f4 v[8:11], v[240:247], v[200:207], v[8:11], v165, v164 op_sel_hi:[0,0,0]
	s_setprio 0
	s_barrier
	ds_read_b128 v[208:211], v128
	ds_read_b128 v[212:215], v129
	ds_read_b128 v[224:227], v128 offset:2048
	ds_read_b128 v[228:231], v129 offset:2048
	ds_read_b128 v[232:235], v130
	ds_read_b128 v[236:239], v131
	ds_read_b128 v[240:243], v130 offset:2048
	ds_read_b128 v[244:247], v131 offset:2048
	ds_read_b128 v[138:141], v135 offset:32784
	ds_read_b128 v[142:145], v136 offset:32784
	ds_read_b128 v[146:149], v135 offset:34832
	ds_read_b128 v[150:153], v136 offset:34832
	ds_read_b128 v[154:157], v135 offset:36880
	ds_read_b128 v[158:161], v136 offset:36880
	ds_read_b128 v[168:171], v135 offset:38928
	ds_read_b128 v[172:175], v136 offset:38928
	ds_read_b128 v[176:179], v135 offset:49168
	ds_read_b128 v[180:183], v136 offset:49168
	ds_read_b128 v[184:187], v135 offset:51216
	ds_read_b128 v[188:191], v136 offset:51216
	ds_read_b128 v[192:195], v135 offset:53264
	ds_read_b128 v[196:199], v136 offset:53264
	ds_read_b128 v[200:203], v135 offset:55312
	ds_read_b128 v[204:207], v136 offset:55312
	s_waitcnt lgkmcnt(0)
	s_cmp_ge_u32 s68, 14
	s_cbranch_scc1 .Lkl_m2pre_y_nd1
	s_lshl_b32 s63, s68, 7
	s_addk_i32 s63, 0x180
	s_add_i32 s64, s63, 0x20000
	s_add_i32 s65, s63, 0x40000
	s_add_i32 s66, s63, 0x60000
	s_mov_b32 m0, s39
	s_nop 0
	buffer_load_dwordx4 v134, s[4:7], s63 offen lds
	s_mov_b32 m0, s49
	s_nop 0
	buffer_load_dwordx4 v162, s[8:11], s63 offen lds
	s_mov_b32 m0, s60
	s_nop 0
	buffer_load_dwordx4 v134, s[4:7], s64 offen lds
	s_mov_b32 m0, s61
	s_nop 0
	buffer_load_dwordx4 v163, s[8:11], s63 offen lds
	s_mov_b32 m0, s50
	s_nop 0
	buffer_load_dwordx4 v134, s[4:7], s65 offen lds
	s_mov_b32 m0, s24
	s_nop 0
	buffer_load_dwordx4 v166, s[8:11], s63 offen lds
	s_mov_b32 m0, s62
	s_nop 0
	buffer_load_dwordx4 v134, s[4:7], s66 offen lds
	s_mov_b32 m0, s51
	s_nop 0
	buffer_load_dwordx4 v167, s[8:11], s63 offen lds
	s_waitcnt vmcnt(8)
	s_branch .Lkl_m2pre_y_nd1_j

; #define G_WAIT_V(n) asm volatile("s_waitcnt vmcnt(" #n ")" ::: "memory")
; #define G_BAR() __builtin_amdgcn_s_barrier()
; #define G_SCHED() __builtin_amdgcn_sched_barrier(0)
; #define D_STAGE_A(slot, half, kt) D_STAGE(rsA, voffA, slot, half, kt)
; #define D_STAGE_B(slot, half, kt) D_STAGE(rsB, voffB, slot, half, kt)
; #define D_LDA(dst, slot) do { _Pragma("unroll") for (int m = 0; m < 4; ++m) _Pragma("unroll") for (int k = 0; k < 2; ++k) \
;     dst[m][k] = *(const LDS_AS bf16x8*)(lds + (slot) + aoff + m * 2048 + k * 1024); } while (0)
; #define D_LDB(dst, slot) do { _Pragma("unroll") for (int n = 0; n < 2; ++n) _Pragma("unroll") for (int k = 0; k < 2; ++k) \
;     dst[n][k] = *(const LDS_AS bf16x8*)(lds + (slot) + boff + n * 2048 + k * 1024); } while (0)
; #define D_MMA(ai, bj, At, Bf) do { __builtin_amdgcn_s_setprio(1); _Pragma("unroll") for (int m = 0; m < 4; ++m) _Pragma("unroll") for (int n = 0; n < 2; ++n) _Pragma("unroll") for (int k = 0; k < 2; ++k) \
;     acc[ai][bj][m][n] = __builtin_amdgcn_mfma_f32_16x16x32_bf16(Bf[n][k], At[m][k], acc[ai][bj][m][n], 0, 0, 0); __builtin_amdgcn_s_setprio(0); } while (0)
; #define D_WAIT_L(n) asm volatile("s_waitcnt lgkmcnt(" #n ")" ::: "memory")
; #define D_STAGE_A(slot, half, kt) D_STAGE(rsA, voffA, slot, half, kt)
; #define D_STAGE_B(slot, half, kt) do { _Pragma("unroll") for (int _i = 0; _i < 2; ++_i) { const unsigned _m0 = ldsw + (unsigned)((slot) + _i * 8192); const unsigned _so = (unsigned)(kt) * 128u + (half) * bt_half + _i * bt_piece; \
;     asm volatile("s_mov_b32 m0, %0\n\ts_nop 4\n\tbuffer_load_dwordx4 %1, %2, %3 offen lds" :: "s"(_m0), "v"(voffB0), "s"(rsB), "s"(_so) : "m0", "memory"); } } while (0)
; #define D_WAIT_L(n) asm volatile("s_waitcnt lgkmcnt(" #n ")" ::: "memory")
;     ...
;     D_LDB(B0, G_SB(1, 0)); G_SCHED(); D_LDA(At, G_SA(1, 0)); D_STAGE_A(G_SA(0, 1), 1, t2);
;     D_WAIT_L(8); G_BAR(); D_WAIT_L(0); G_SCHED(); D_MMA(0, 0, At, B0); G_BAR(); G_SCHED();
;     D_LDB(B1, G_SB(1, 1)); D_STAGE_B(G_SB(1, 0), 0, t3);
;     G_BAR(); D_WAIT_L(0); G_SCHED(); D_MMA(0, 1, At, B1); G_BAR(); G_SCHED();
;     D_LDA(At, G_SA(1, 1)); D_STAGE_A(G_SA(1, 0), 0, t3);
;     G_BAR(); D_WAIT_L(0); G_SCHED(); D_MMA(1, 0, At, B0); G_BAR(); G_SCHED();
;     D_STAGE_B(G_SB(1, 1), 1, t3);
;     G_WAIT_V(6); G_BAR(); G_SCHED(); D_MMA(1, 1, At, B1); G_BAR(); G_SCHED();
.Lkl_m2pre_y_nd1_j:
	s_barrier
	s_setprio 1
	v_mfma_scale_f32_16x16x128_f8f6f4 v[124:127], v[208:215], v[138:145], v[124:127], v165, v164 op_sel_hi:[0,0,0]
	v_mfma_scale_f32_16x16x128_f8f6f4 v[120:123], v[224:231], v[138:145], v[120:123], v165, v164 op_sel_hi:[0,0,0]
	v_mfma_scale_f32_16x16x128_f8f6f4 v[108:111], v[208:215], v[146:153], v[108:111], v165, v164 op_sel_hi:[0,0,0]
	v_mfma_scale_f32_16x16x128_f8f6f4 v[100:103], v[224:231], v[146:153], v[100:103], v165, v164 op_sel_hi:[0,0,0]
	v_mfma_scale_f32_16x16x128_f8f6f4 v[84:87], v[208:215], v[154:161], v[84:87], v165, v164 op_sel_hi:[0,0,0]
	v_mfma_scale_f32_16x16x128_f8f6f4 v[80:83], v[224:231], v[154:161], v[80:83], v165, v164 op_sel_hi:[0,0,0]
	v_mfma_scale_f32_16x16x128_f8f6f4 v[220:223], v[208:215], v[168:175], v[220:223], v165, v164 op_sel_hi:[0,0,0]
	v_mfma_scale_f32_16x16x128_f8f6f4 v[48:51], v[224:231], v[168:175], v[48:51], v165, v164 op_sel_hi:[0,0,0]
	v_mfma_scale_f32_16x16x128_f8f6f4 v[116:119], v[232:239], v[138:145], v[116:119], v165, v164 op_sel_hi:[0,0,0]
	v_mfma_scale_f32_16x16x128_f8f6f4 v[112:115], v[240:247], v[138:145], v[112:115], v165, v164 op_sel_hi:[0,0,0]
	v_mfma_scale_f32_16x16x128_f8f6f4 v[104:107], v[232:239], v[146:153], v[104:107], v165, v164 op_sel_hi:[0,0,0]
	v_mfma_scale_f32_16x16x128_f8f6f4 v[96:99], v[240:247], v[146:153], v[96:99], v165, v164 op_sel_hi:[0,0,0]
	v_mfma_scale_f32_16x16x128_f8f6f4 v[92:95], v[232:239], v[154:161], v[92:95], v165, v164 op_sel_hi:[0,0,0]
	v_mfma_scale_f32_16x16x128_f8f6f4 v[88:91], v[240:247], v[154:161], v[88:91], v165, v164 op_sel_hi:[0,0,0]
	v_mfma_scale_f32_16x16x128_f8f6f4 v[76:79], v[232:239], v[168:175], v[76:79], v165, v164 op_sel_hi:[0,0,0]
	v_mfma_scale_f32_16x16x128_f8f6f4 v[72:75], v[240:247], v[168:175], v[72:75], v165, v164 op_sel_hi:[0,0,0]
	v_mfma_scale_f32_16x16x128_f8f6f4 v[56:59], v[208:215], v[176:183], v[56:59], v165, v164 op_sel_hi:[0,0,0]
	v_mfma_scale_f32_16x16x128_f8f6f4 v[52:55], v[224:231], v[176:183], v[52:55], v165, v164 op_sel_hi:[0,0,0]
	v_mfma_scale_f32_16x16x128_f8f6f4 v[36:39], v[208:215], v[184:191], v[36:39], v165, v164 op_sel_hi:[0,0,0]
	v_mfma_scale_f32_16x16x128_f8f6f4 v[32:35], v[224:231], v[184:191], v[32:35], v165, v164 op_sel_hi:[0,0,0]
	v_mfma_scale_f32_16x16x128_f8f6f4 v[20:23], v[208:215], v[192:199], v[20:23], v165, v164 op_sel_hi:[0,0,0]
	v_mfma_scale_f32_16x16x128_f8f6f4 v[16:19], v[224:231], v[192:199], v[16:19], v165, v164 op_sel_hi:[0,0,0]
	v_mfma_scale_f32_16x16x128_f8f6f4 v[4:7], v[208:215], v[200:207], v[4:7], v165, v164 op_sel_hi:[0,0,0]
	v_mfma_scale_f32_16x16x128_f8f6f4 v[0:3], v[224:231], v[200:207], v[0:3], v165, v164 op_sel_hi:[0,0,0]
	v_mfma_scale_f32_16x16x128_f8f6f4 v[64:67], v[232:239], v[176:183], v[64:67], v165, v164 op_sel_hi:[0,0,0]
	v_mfma_scale_f32_16x16x128_f8f6f4 v[60:63], v[240:247], v[176:183], v[60:63], v165, v164 op_sel_hi:[0,0,0]
	v_mfma_scale_f32_16x16x128_f8f6f4 v[44:47], v[232:239], v[184:191], v[44:47], v165, v164 op_sel_hi:[0,0,0]
	v_mfma_scale_f32_16x16x128_f8f6f4 v[40:43], v[240:247], v[184:191], v[40:43], v165, v164 op_sel_hi:[0,0,0]
	v_mfma_scale_f32_16x16x128_f8f6f4 v[28:31], v[232:239], v[192:199], v[28:31], v165, v164 op_sel_hi:[0,0,0]
	v_mfma_scale_f32_16x16x128_f8f6f4 v[24:27], v[240:247], v[192:199], v[24:27], v165, v164 op_sel_hi:[0,0,0]
	v_mfma_scale_f32_16x16x128_f8f6f4 v[12:15], v[232:239], v[200:207], v[12:15], v165, v164 op_sel_hi:[0,0,0]
	v_mfma_scale_f32_16x16x128_f8f6f4 v[8:11], v[240:247], v[200:207], v[8:11], v165, v164 op_sel_hi:[0,0,0]
	s_setprio 0
	s_barrier
	s_add_i32 s68, s68, 2
	s_cmp_lt_u32 s68, 16
	s_cbranch_scc1 .Lkl_m2pre_yl
